# speedup vs baseline: 1.0110x; 1.0078x over previous
.LBB2_27:
	ds_read2st64_b32 v[10:11], v8 offset1:1
	v_add_u32_e32 v7, 16, v7
	v_cmp_lt_u32_e32 vcc, 3, v7
	s_or_b64 s[0:1], vcc, s[0:1]
	s_waitcnt lgkmcnt(0)
	v_max_f32_e32 v9, v11, v11
	v_max_f32_e32 v12, v10, v10
	v_max_f32_e32 v9, v12, v9
	s_nop 1
	v_max_f32_dpp v9, v9, v9 quad_perm:[1,0,3,2] row_mask:0xf bank_mask:0xf
	s_nop 1
	v_max_f32_dpp v9, v9, v9 quad_perm:[2,3,0,1] row_mask:0xf bank_mask:0xf
	s_nop 1
	v_max_f32_dpp v9, v9, v9 row_half_mirror row_mask:0xf bank_mask:0xf
	s_nop 1
	v_max_f32_dpp v9, v9, v9 row_mirror row_mask:0xf bank_mask:0xf
	s_nop 1
	v_readlane_b32 s30, v9, 0
	v_readlane_b32 s31, v9, 16
	v_readlane_b32 s32, v9, 32
	v_readlane_b32 s33, v9, 48
	v_mov_b32_e32 v9, s30
	v_max_f32_e32 v9, s31, v9
	v_max_f32_e32 v9, s32, v9
	v_max_f32_e32 v9, s33, v9
	v_sub_f32_e32 v10, v10, v9
	v_sub_f32_e32 v9, v11, v9
	v_mul_f32_e32 v10, 0x3fb8aa3b, v10
	v_mul_f32_e32 v9, 0x3fb8aa3b, v9
	v_exp_f32_e32 v10, v10
	v_exp_f32_e32 v9, v9
	s_nop 0
	v_add_f32_e32 v11, v10, v9
	s_nop 1
	v_add_f32_dpp v11, v11, v11 quad_perm:[1,0,3,2] row_mask:0xf bank_mask:0xf
	s_nop 1
	v_add_f32_dpp v11, v11, v11 quad_perm:[2,3,0,1] row_mask:0xf bank_mask:0xf
	s_nop 1
	v_add_f32_dpp v11, v11, v11 row_half_mirror row_mask:0xf bank_mask:0xf
	s_nop 1
	v_add_f32_dpp v11, v11, v11 row_mirror row_mask:0xf bank_mask:0xf
	s_nop 1
	v_readlane_b32 s30, v11, 0
	v_readlane_b32 s31, v11, 16
	v_readlane_b32 s32, v11, 32
	v_readlane_b32 s33, v11, 48
	v_mov_b32_e32 v11, s30
	v_add_f32_e32 v11, s31, v11
	v_add_f32_e32 v11, s32, v11
	v_add_f32_e32 v11, s33, v11
	v_div_scale_f32 v12, s[4:5], v11, v11, 1.0
	v_rcp_f32_e32 v13, v12
	v_div_scale_f32 v14, vcc, 1.0, v11, 1.0
	v_fma_f32 v15, -v12, v13, 1.0
	v_fmac_f32_e32 v13, v15, v13
	v_mul_f32_e32 v15, v14, v13
	v_fma_f32 v16, -v12, v15, v14
	v_fmac_f32_e32 v15, v16, v13
	v_fma_f32 v12, -v12, v15, v14
	v_div_fmas_f32 v12, v12, v13, v15
	v_div_fixup_f32 v11, v12, v11, 1.0
	v_mul_f32_e32 v10, v10, v11
	v_mul_f32_e32 v9, v9, v11
	ds_write2st64_b32 v8, v10, v9 offset1:1
	v_add_u32_e32 v8, 0x2000, v8
	s_andn2_b64 exec, exec, s[0:1]
	s_cbranch_execnz .LBB2_27
	s_or_b64 exec, exec, s[0:1]
	s_waitcnt lgkmcnt(0)
	s_barrier
	v_readfirstlane_b32 s4, v0
	s_lshr_b32 s4, s4, 6
	s_cmp_gt_u32 s4, 14
	s_cbranch_scc1 .Latt3_join
	s_cmp_gt_u32 s4, 9
	s_cbranch_scc1 .Latt3_hh
	s_movk_i32 s5, 0x258
	v_cmp_gt_u32_e32 vcc, s5, v0
	s_and_saveexec_b64 s[6:7], vcc
	v_mul_u32_u24_e32 v124, 0x1b5, v0
	v_lshrrev_b32_e32 v124, 16, v124
	v_mul_u32_u24_e32 v1, 0x96, v124
	v_sub_u32_e32 v1, v0, v1
	v_mul_u32_u24_e32 v125, 0x36a, v1
	v_lshrrev_b32_e32 v125, 16, v125
	v_mul_u32_u24_e32 v2, 0x4b, v125
	v_sub_u32_e32 v123, v1, v2
	s_mul_i32 s8, s22, 0x25800
	s_add_u32 s8, s2, s8
	s_addc_u32 s9, s3, 0
	v_mul_u32_u24_e32 v2, 0x9600, v124
	v_lshl_add_u32 v2, v123, 4, v2
	v_mov_b32_e32 v3, 0
	v_lshl_add_u64 v[120:121], s[8:9], 0, v[2:3]
	v_lshlrev_b32_e32 v122, 12, v125
	v_lshl_add_u32 v122, v124, 7, v122
	v_add_u32_e32 v122, 0xc800, v122
	v_mul_u32_u24_e32 v126, 0x258, v125
	v_add_u32_e32 v126, v126, v123
	v_add_u32_e32 v126, 0x12c, v126
	v_lshlrev_b32_e32 v126, 4, v126
	s_mov_b64 s[10:11], 0x960
	v_mov_b32_e32 v4, 0
	v_mov_b32_e32 v5, 0
	v_mov_b32_e32 v6, 0
	v_mov_b32_e32 v7, 0
	v_mov_b32_e32 v8, 0
	v_mov_b32_e32 v9, 0
	v_mov_b32_e32 v10, 0
	v_mov_b32_e32 v11, 0
	v_mov_b32_e32 v12, 0
	v_mov_b32_e32 v13, 0
	v_mov_b32_e32 v14, 0
	v_mov_b32_e32 v15, 0
	v_mov_b32_e32 v16, 0
	v_mov_b32_e32 v17, 0
	v_mov_b32_e32 v18, 0
	v_mov_b32_e32 v19, 0
	v_mov_b32_e32 v20, 0
	v_mov_b32_e32 v21, 0
	v_mov_b32_e32 v22, 0
	v_mov_b32_e32 v23, 0
	v_mov_b32_e32 v24, 0
	v_mov_b32_e32 v25, 0
	v_mov_b32_e32 v26, 0
	v_mov_b32_e32 v27, 0
	v_mov_b32_e32 v28, 0
	v_mov_b32_e32 v29, 0
	v_mov_b32_e32 v30, 0
	v_mov_b32_e32 v31, 0
	v_mov_b32_e32 v32, 0
	v_mov_b32_e32 v33, 0
	v_mov_b32_e32 v34, 0
	v_mov_b32_e32 v35, 0
	ds_read_b64 v[88:89], v122
	ds_read_b64 v[90:91], v122 offset:512
	ds_read_b64 v[92:93], v122 offset:1024
	ds_read_b64 v[94:95], v122 offset:1536
	ds_read_b64 v[96:97], v122 offset:2048
	ds_read_b64 v[98:99], v122 offset:2560
	ds_read_b64 v[100:101], v122 offset:3072
	ds_read_b64 v[102:103], v122 offset:3584
	global_load_dwordx4 v[36:39], v[120:121], off
	global_load_dwordx4 v[40:43], v[120:121], off offset:1200
	s_nop 0
	v_lshl_add_u64 v[120:121], v[120:121], 0, s[10:11]
	global_load_dwordx4 v[44:47], v[120:121], off
	global_load_dwordx4 v[48:51], v[120:121], off offset:1200
	s_nop 0
	v_lshl_add_u64 v[120:121], v[120:121], 0, s[10:11]
	global_load_dwordx4 v[52:55], v[120:121], off
	global_load_dwordx4 v[56:59], v[120:121], off offset:1200
	s_nop 0
	v_lshl_add_u64 v[120:121], v[120:121], 0, s[10:11]
	global_load_dwordx4 v[60:63], v[120:121], off
	global_load_dwordx4 v[64:67], v[120:121], off offset:1200
	s_nop 0
	v_lshl_add_u64 v[120:121], v[120:121], 0, s[10:11]
	global_load_dwordx4 v[72:75], v[120:121], off
	global_load_dwordx4 v[76:79], v[120:121], off offset:1200
	s_nop 0
	v_lshl_add_u64 v[120:121], v[120:121], 0, s[10:11]
	global_load_dwordx4 v[80:83], v[120:121], off
	global_load_dwordx4 v[84:87], v[120:121], off offset:1200
	ds_read_b64 v[104:105], v122 offset:8
	ds_read_b64 v[106:107], v122 offset:520
	ds_read_b64 v[108:109], v122 offset:1032
	ds_read_b64 v[110:111], v122 offset:1544
	ds_read_b64 v[112:113], v122 offset:2056
	ds_read_b64 v[114:115], v122 offset:2568
	ds_read_b64 v[116:117], v122 offset:3080
	ds_read_b64 v[118:119], v122 offset:3592
	v_lshl_add_u64 v[120:121], v[120:121], 0, s[10:11]
	s_waitcnt vmcnt(10) lgkmcnt(8)
	v_pk_fma_f32 v[4:5], v[88:89], v[36:37], v[4:5] op_sel_hi:[0,1,1]
	v_pk_fma_f32 v[6:7], v[88:89], v[38:39], v[6:7] op_sel_hi:[0,1,1]
	v_pk_fma_f32 v[8:9], v[90:91], v[36:37], v[8:9] op_sel_hi:[0,1,1]
	v_pk_fma_f32 v[10:11], v[90:91], v[38:39], v[10:11] op_sel_hi:[0,1,1]
	v_pk_fma_f32 v[12:13], v[92:93], v[36:37], v[12:13] op_sel_hi:[0,1,1]
	v_pk_fma_f32 v[14:15], v[92:93], v[38:39], v[14:15] op_sel_hi:[0,1,1]
	v_pk_fma_f32 v[16:17], v[94:95], v[36:37], v[16:17] op_sel_hi:[0,1,1]
	v_pk_fma_f32 v[18:19], v[94:95], v[38:39], v[18:19] op_sel_hi:[0,1,1]
	v_pk_fma_f32 v[20:21], v[96:97], v[36:37], v[20:21] op_sel_hi:[0,1,1]
	v_pk_fma_f32 v[22:23], v[96:97], v[38:39], v[22:23] op_sel_hi:[0,1,1]
	v_pk_fma_f32 v[24:25], v[98:99], v[36:37], v[24:25] op_sel_hi:[0,1,1]
	v_pk_fma_f32 v[26:27], v[98:99], v[38:39], v[26:27] op_sel_hi:[0,1,1]
	v_pk_fma_f32 v[28:29], v[100:101], v[36:37], v[28:29] op_sel_hi:[0,1,1]
	v_pk_fma_f32 v[30:31], v[100:101], v[38:39], v[30:31] op_sel_hi:[0,1,1]
	v_pk_fma_f32 v[32:33], v[102:103], v[36:37], v[32:33] op_sel_hi:[0,1,1]
	v_pk_fma_f32 v[34:35], v[102:103], v[38:39], v[34:35] op_sel_hi:[0,1,1]
	v_pk_fma_f32 v[4:5], v[88:89], v[40:41], v[4:5] op_sel:[1,0,0]
	v_pk_fma_f32 v[6:7], v[88:89], v[42:43], v[6:7] op_sel:[1,0,0]
	v_pk_fma_f32 v[8:9], v[90:91], v[40:41], v[8:9] op_sel:[1,0,0]
	v_pk_fma_f32 v[10:11], v[90:91], v[42:43], v[10:11] op_sel:[1,0,0]
	v_pk_fma_f32 v[12:13], v[92:93], v[40:41], v[12:13] op_sel:[1,0,0]
	v_pk_fma_f32 v[14:15], v[92:93], v[42:43], v[14:15] op_sel:[1,0,0]
	v_pk_fma_f32 v[16:17], v[94:95], v[40:41], v[16:17] op_sel:[1,0,0]
	v_pk_fma_f32 v[18:19], v[94:95], v[42:43], v[18:19] op_sel:[1,0,0]
	v_pk_fma_f32 v[20:21], v[96:97], v[40:41], v[20:21] op_sel:[1,0,0]
	v_pk_fma_f32 v[22:23], v[96:97], v[42:43], v[22:23] op_sel:[1,0,0]
	v_pk_fma_f32 v[24:25], v[98:99], v[40:41], v[24:25] op_sel:[1,0,0]
	v_pk_fma_f32 v[26:27], v[98:99], v[42:43], v[26:27] op_sel:[1,0,0]
	v_pk_fma_f32 v[28:29], v[100:101], v[40:41], v[28:29] op_sel:[1,0,0]
	v_pk_fma_f32 v[30:31], v[100:101], v[42:43], v[30:31] op_sel:[1,0,0]
	v_pk_fma_f32 v[32:33], v[102:103], v[40:41], v[32:33] op_sel:[1,0,0]
	v_pk_fma_f32 v[34:35], v[102:103], v[42:43], v[34:35] op_sel:[1,0,0]
	global_load_dwordx4 v[36:39], v[120:121], off
	global_load_dwordx4 v[40:43], v[120:121], off offset:1200
	ds_read_b64 v[88:89], v122 offset:16
	ds_read_b64 v[90:91], v122 offset:528
	ds_read_b64 v[92:93], v122 offset:1040
	ds_read_b64 v[94:95], v122 offset:1552
	ds_read_b64 v[96:97], v122 offset:2064
	ds_read_b64 v[98:99], v122 offset:2576
	ds_read_b64 v[100:101], v122 offset:3088
	ds_read_b64 v[102:103], v122 offset:3600
	v_lshl_add_u64 v[120:121], v[120:121], 0, s[10:11]
	s_waitcnt vmcnt(10) lgkmcnt(8)
	v_pk_fma_f32 v[4:5], v[104:105], v[44:45], v[4:5] op_sel_hi:[0,1,1]
	v_pk_fma_f32 v[6:7], v[104:105], v[46:47], v[6:7] op_sel_hi:[0,1,1]
	v_pk_fma_f32 v[8:9], v[106:107], v[44:45], v[8:9] op_sel_hi:[0,1,1]
	v_pk_fma_f32 v[10:11], v[106:107], v[46:47], v[10:11] op_sel_hi:[0,1,1]
	v_pk_fma_f32 v[12:13], v[108:109], v[44:45], v[12:13] op_sel_hi:[0,1,1]
	v_pk_fma_f32 v[14:15], v[108:109], v[46:47], v[14:15] op_sel_hi:[0,1,1]
	v_pk_fma_f32 v[16:17], v[110:111], v[44:45], v[16:17] op_sel_hi:[0,1,1]
	v_pk_fma_f32 v[18:19], v[110:111], v[46:47], v[18:19] op_sel_hi:[0,1,1]
	v_pk_fma_f32 v[20:21], v[112:113], v[44:45], v[20:21] op_sel_hi:[0,1,1]
	v_pk_fma_f32 v[22:23], v[112:113], v[46:47], v[22:23] op_sel_hi:[0,1,1]
	v_pk_fma_f32 v[24:25], v[114:115], v[44:45], v[24:25] op_sel_hi:[0,1,1]
	v_pk_fma_f32 v[26:27], v[114:115], v[46:47], v[26:27] op_sel_hi:[0,1,1]
	v_pk_fma_f32 v[28:29], v[116:117], v[44:45], v[28:29] op_sel_hi:[0,1,1]
	v_pk_fma_f32 v[30:31], v[116:117], v[46:47], v[30:31] op_sel_hi:[0,1,1]
	v_pk_fma_f32 v[32:33], v[118:119], v[44:45], v[32:33] op_sel_hi:[0,1,1]
	v_pk_fma_f32 v[34:35], v[118:119], v[46:47], v[34:35] op_sel_hi:[0,1,1]
	v_pk_fma_f32 v[4:5], v[104:105], v[48:49], v[4:5] op_sel:[1,0,0]
	v_pk_fma_f32 v[6:7], v[104:105], v[50:51], v[6:7] op_sel:[1,0,0]
	v_pk_fma_f32 v[8:9], v[106:107], v[48:49], v[8:9] op_sel:[1,0,0]
	v_pk_fma_f32 v[10:11], v[106:107], v[50:51], v[10:11] op_sel:[1,0,0]
	v_pk_fma_f32 v[12:13], v[108:109], v[48:49], v[12:13] op_sel:[1,0,0]
	v_pk_fma_f32 v[14:15], v[108:109], v[50:51], v[14:15] op_sel:[1,0,0]
	v_pk_fma_f32 v[16:17], v[110:111], v[48:49], v[16:17] op_sel:[1,0,0]
	v_pk_fma_f32 v[18:19], v[110:111], v[50:51], v[18:19] op_sel:[1,0,0]
	v_pk_fma_f32 v[20:21], v[112:113], v[48:49], v[20:21] op_sel:[1,0,0]
	v_pk_fma_f32 v[22:23], v[112:113], v[50:51], v[22:23] op_sel:[1,0,0]
	v_pk_fma_f32 v[24:25], v[114:115], v[48:49], v[24:25] op_sel:[1,0,0]
	v_pk_fma_f32 v[26:27], v[114:115], v[50:51], v[26:27] op_sel:[1,0,0]
	v_pk_fma_f32 v[28:29], v[116:117], v[48:49], v[28:29] op_sel:[1,0,0]
	v_pk_fma_f32 v[30:31], v[116:117], v[50:51], v[30:31] op_sel:[1,0,0]
	v_pk_fma_f32 v[32:33], v[118:119], v[48:49], v[32:33] op_sel:[1,0,0]
	v_pk_fma_f32 v[34:35], v[118:119], v[50:51], v[34:35] op_sel:[1,0,0]
	global_load_dwordx4 v[44:47], v[120:121], off
	global_load_dwordx4 v[48:51], v[120:121], off offset:1200
	ds_read_b64 v[104:105], v122 offset:24
	ds_read_b64 v[106:107], v122 offset:536
	ds_read_b64 v[108:109], v122 offset:1048
	ds_read_b64 v[110:111], v122 offset:1560
	ds_read_b64 v[112:113], v122 offset:2072
	ds_read_b64 v[114:115], v122 offset:2584
	ds_read_b64 v[116:117], v122 offset:3096
	ds_read_b64 v[118:119], v122 offset:3608
	v_lshl_add_u64 v[120:121], v[120:121], 0, s[10:11]
	s_waitcnt vmcnt(10) lgkmcnt(8)
	v_pk_fma_f32 v[4:5], v[88:89], v[52:53], v[4:5] op_sel_hi:[0,1,1]
	v_pk_fma_f32 v[6:7], v[88:89], v[54:55], v[6:7] op_sel_hi:[0,1,1]
	v_pk_fma_f32 v[8:9], v[90:91], v[52:53], v[8:9] op_sel_hi:[0,1,1]
	v_pk_fma_f32 v[10:11], v[90:91], v[54:55], v[10:11] op_sel_hi:[0,1,1]
	v_pk_fma_f32 v[12:13], v[92:93], v[52:53], v[12:13] op_sel_hi:[0,1,1]
	v_pk_fma_f32 v[14:15], v[92:93], v[54:55], v[14:15] op_sel_hi:[0,1,1]
	v_pk_fma_f32 v[16:17], v[94:95], v[52:53], v[16:17] op_sel_hi:[0,1,1]
	v_pk_fma_f32 v[18:19], v[94:95], v[54:55], v[18:19] op_sel_hi:[0,1,1]
	v_pk_fma_f32 v[20:21], v[96:97], v[52:53], v[20:21] op_sel_hi:[0,1,1]
	v_pk_fma_f32 v[22:23], v[96:97], v[54:55], v[22:23] op_sel_hi:[0,1,1]
	v_pk_fma_f32 v[24:25], v[98:99], v[52:53], v[24:25] op_sel_hi:[0,1,1]
	v_pk_fma_f32 v[26:27], v[98:99], v[54:55], v[26:27] op_sel_hi:[0,1,1]
	v_pk_fma_f32 v[28:29], v[100:101], v[52:53], v[28:29] op_sel_hi:[0,1,1]
	v_pk_fma_f32 v[30:31], v[100:101], v[54:55], v[30:31] op_sel_hi:[0,1,1]
	v_pk_fma_f32 v[32:33], v[102:103], v[52:53], v[32:33] op_sel_hi:[0,1,1]
	v_pk_fma_f32 v[34:35], v[102:103], v[54:55], v[34:35] op_sel_hi:[0,1,1]
	v_pk_fma_f32 v[4:5], v[88:89], v[56:57], v[4:5] op_sel:[1,0,0]
	v_pk_fma_f32 v[6:7], v[88:89], v[58:59], v[6:7] op_sel:[1,0,0]
	v_pk_fma_f32 v[8:9], v[90:91], v[56:57], v[8:9] op_sel:[1,0,0]
	v_pk_fma_f32 v[10:11], v[90:91], v[58:59], v[10:11] op_sel:[1,0,0]
	v_pk_fma_f32 v[12:13], v[92:93], v[56:57], v[12:13] op_sel:[1,0,0]
	v_pk_fma_f32 v[14:15], v[92:93], v[58:59], v[14:15] op_sel:[1,0,0]
	v_pk_fma_f32 v[16:17], v[94:95], v[56:57], v[16:17] op_sel:[1,0,0]
	v_pk_fma_f32 v[18:19], v[94:95], v[58:59], v[18:19] op_sel:[1,0,0]
	v_pk_fma_f32 v[20:21], v[96:97], v[56:57], v[20:21] op_sel:[1,0,0]
	v_pk_fma_f32 v[22:23], v[96:97], v[58:59], v[22:23] op_sel:[1,0,0]
	v_pk_fma_f32 v[24:25], v[98:99], v[56:57], v[24:25] op_sel:[1,0,0]
	v_pk_fma_f32 v[26:27], v[98:99], v[58:59], v[26:27] op_sel:[1,0,0]
	v_pk_fma_f32 v[28:29], v[100:101], v[56:57], v[28:29] op_sel:[1,0,0]
	v_pk_fma_f32 v[30:31], v[100:101], v[58:59], v[30:31] op_sel:[1,0,0]
	v_pk_fma_f32 v[32:33], v[102:103], v[56:57], v[32:33] op_sel:[1,0,0]
	v_pk_fma_f32 v[34:35], v[102:103], v[58:59], v[34:35] op_sel:[1,0,0]
	global_load_dwordx4 v[52:55], v[120:121], off
	global_load_dwordx4 v[56:59], v[120:121], off offset:1200
	ds_read_b64 v[88:89], v122 offset:32
	ds_read_b64 v[90:91], v122 offset:544
	ds_read_b64 v[92:93], v122 offset:1056
	ds_read_b64 v[94:95], v122 offset:1568
	ds_read_b64 v[96:97], v122 offset:2080
	ds_read_b64 v[98:99], v122 offset:2592
	ds_read_b64 v[100:101], v122 offset:3104
	ds_read_b64 v[102:103], v122 offset:3616
	v_lshl_add_u64 v[120:121], v[120:121], 0, s[10:11]
	s_waitcnt vmcnt(10) lgkmcnt(8)
	v_pk_fma_f32 v[4:5], v[104:105], v[60:61], v[4:5] op_sel_hi:[0,1,1]
	v_pk_fma_f32 v[6:7], v[104:105], v[62:63], v[6:7] op_sel_hi:[0,1,1]
	v_pk_fma_f32 v[8:9], v[106:107], v[60:61], v[8:9] op_sel_hi:[0,1,1]
	v_pk_fma_f32 v[10:11], v[106:107], v[62:63], v[10:11] op_sel_hi:[0,1,1]
	v_pk_fma_f32 v[12:13], v[108:109], v[60:61], v[12:13] op_sel_hi:[0,1,1]
	v_pk_fma_f32 v[14:15], v[108:109], v[62:63], v[14:15] op_sel_hi:[0,1,1]
	v_pk_fma_f32 v[16:17], v[110:111], v[60:61], v[16:17] op_sel_hi:[0,1,1]
	v_pk_fma_f32 v[18:19], v[110:111], v[62:63], v[18:19] op_sel_hi:[0,1,1]
	v_pk_fma_f32 v[20:21], v[112:113], v[60:61], v[20:21] op_sel_hi:[0,1,1]
	v_pk_fma_f32 v[22:23], v[112:113], v[62:63], v[22:23] op_sel_hi:[0,1,1]
	v_pk_fma_f32 v[24:25], v[114:115], v[60:61], v[24:25] op_sel_hi:[0,1,1]
	v_pk_fma_f32 v[26:27], v[114:115], v[62:63], v[26:27] op_sel_hi:[0,1,1]
	v_pk_fma_f32 v[28:29], v[116:117], v[60:61], v[28:29] op_sel_hi:[0,1,1]
	v_pk_fma_f32 v[30:31], v[116:117], v[62:63], v[30:31] op_sel_hi:[0,1,1]
	v_pk_fma_f32 v[32:33], v[118:119], v[60:61], v[32:33] op_sel_hi:[0,1,1]
	v_pk_fma_f32 v[34:35], v[118:119], v[62:63], v[34:35] op_sel_hi:[0,1,1]
	v_pk_fma_f32 v[4:5], v[104:105], v[64:65], v[4:5] op_sel:[1,0,0]
	v_pk_fma_f32 v[6:7], v[104:105], v[66:67], v[6:7] op_sel:[1,0,0]
	v_pk_fma_f32 v[8:9], v[106:107], v[64:65], v[8:9] op_sel:[1,0,0]
	v_pk_fma_f32 v[10:11], v[106:107], v[66:67], v[10:11] op_sel:[1,0,0]
	v_pk_fma_f32 v[12:13], v[108:109], v[64:65], v[12:13] op_sel:[1,0,0]
	v_pk_fma_f32 v[14:15], v[108:109], v[66:67], v[14:15] op_sel:[1,0,0]
	v_pk_fma_f32 v[16:17], v[110:111], v[64:65], v[16:17] op_sel:[1,0,0]
	v_pk_fma_f32 v[18:19], v[110:111], v[66:67], v[18:19] op_sel:[1,0,0]
	v_pk_fma_f32 v[20:21], v[112:113], v[64:65], v[20:21] op_sel:[1,0,0]
	v_pk_fma_f32 v[22:23], v[112:113], v[66:67], v[22:23] op_sel:[1,0,0]
	v_pk_fma_f32 v[24:25], v[114:115], v[64:65], v[24:25] op_sel:[1,0,0]
	v_pk_fma_f32 v[26:27], v[114:115], v[66:67], v[26:27] op_sel:[1,0,0]
	v_pk_fma_f32 v[28:29], v[116:117], v[64:65], v[28:29] op_sel:[1,0,0]
	v_pk_fma_f32 v[30:31], v[116:117], v[66:67], v[30:31] op_sel:[1,0,0]
	v_pk_fma_f32 v[32:33], v[118:119], v[64:65], v[32:33] op_sel:[1,0,0]
	v_pk_fma_f32 v[34:35], v[118:119], v[66:67], v[34:35] op_sel:[1,0,0]
	global_load_dwordx4 v[60:63], v[120:121], off
	global_load_dwordx4 v[64:67], v[120:121], off offset:1200
	ds_read_b64 v[104:105], v122 offset:40
	ds_read_b64 v[106:107], v122 offset:552
	ds_read_b64 v[108:109], v122 offset:1064
	ds_read_b64 v[110:111], v122 offset:1576
	ds_read_b64 v[112:113], v122 offset:2088
	ds_read_b64 v[114:115], v122 offset:2600
	ds_read_b64 v[116:117], v122 offset:3112
	ds_read_b64 v[118:119], v122 offset:3624
	v_lshl_add_u64 v[120:121], v[120:121], 0, s[10:11]
	s_waitcnt vmcnt(10) lgkmcnt(8)
	v_pk_fma_f32 v[4:5], v[88:89], v[72:73], v[4:5] op_sel_hi:[0,1,1]
	v_pk_fma_f32 v[6:7], v[88:89], v[74:75], v[6:7] op_sel_hi:[0,1,1]
	v_pk_fma_f32 v[8:9], v[90:91], v[72:73], v[8:9] op_sel_hi:[0,1,1]
	v_pk_fma_f32 v[10:11], v[90:91], v[74:75], v[10:11] op_sel_hi:[0,1,1]
	v_pk_fma_f32 v[12:13], v[92:93], v[72:73], v[12:13] op_sel_hi:[0,1,1]
	v_pk_fma_f32 v[14:15], v[92:93], v[74:75], v[14:15] op_sel_hi:[0,1,1]
	v_pk_fma_f32 v[16:17], v[94:95], v[72:73], v[16:17] op_sel_hi:[0,1,1]
	v_pk_fma_f32 v[18:19], v[94:95], v[74:75], v[18:19] op_sel_hi:[0,1,1]
	v_pk_fma_f32 v[20:21], v[96:97], v[72:73], v[20:21] op_sel_hi:[0,1,1]
	v_pk_fma_f32 v[22:23], v[96:97], v[74:75], v[22:23] op_sel_hi:[0,1,1]
	v_pk_fma_f32 v[24:25], v[98:99], v[72:73], v[24:25] op_sel_hi:[0,1,1]
	v_pk_fma_f32 v[26:27], v[98:99], v[74:75], v[26:27] op_sel_hi:[0,1,1]
	v_pk_fma_f32 v[28:29], v[100:101], v[72:73], v[28:29] op_sel_hi:[0,1,1]
	v_pk_fma_f32 v[30:31], v[100:101], v[74:75], v[30:31] op_sel_hi:[0,1,1]
	v_pk_fma_f32 v[32:33], v[102:103], v[72:73], v[32:33] op_sel_hi:[0,1,1]
	v_pk_fma_f32 v[34:35], v[102:103], v[74:75], v[34:35] op_sel_hi:[0,1,1]
	v_pk_fma_f32 v[4:5], v[88:89], v[76:77], v[4:5] op_sel:[1,0,0]
	v_pk_fma_f32 v[6:7], v[88:89], v[78:79], v[6:7] op_sel:[1,0,0]
	v_pk_fma_f32 v[8:9], v[90:91], v[76:77], v[8:9] op_sel:[1,0,0]
	v_pk_fma_f32 v[10:11], v[90:91], v[78:79], v[10:11] op_sel:[1,0,0]
	v_pk_fma_f32 v[12:13], v[92:93], v[76:77], v[12:13] op_sel:[1,0,0]
	v_pk_fma_f32 v[14:15], v[92:93], v[78:79], v[14:15] op_sel:[1,0,0]
	v_pk_fma_f32 v[16:17], v[94:95], v[76:77], v[16:17] op_sel:[1,0,0]
	v_pk_fma_f32 v[18:19], v[94:95], v[78:79], v[18:19] op_sel:[1,0,0]
	v_pk_fma_f32 v[20:21], v[96:97], v[76:77], v[20:21] op_sel:[1,0,0]
	v_pk_fma_f32 v[22:23], v[96:97], v[78:79], v[22:23] op_sel:[1,0,0]
	v_pk_fma_f32 v[24:25], v[98:99], v[76:77], v[24:25] op_sel:[1,0,0]
	v_pk_fma_f32 v[26:27], v[98:99], v[78:79], v[26:27] op_sel:[1,0,0]
	v_pk_fma_f32 v[28:29], v[100:101], v[76:77], v[28:29] op_sel:[1,0,0]
	v_pk_fma_f32 v[30:31], v[100:101], v[78:79], v[30:31] op_sel:[1,0,0]
	v_pk_fma_f32 v[32:33], v[102:103], v[76:77], v[32:33] op_sel:[1,0,0]
	v_pk_fma_f32 v[34:35], v[102:103], v[78:79], v[34:35] op_sel:[1,0,0]
	global_load_dwordx4 v[72:75], v[120:121], off
	global_load_dwordx4 v[76:79], v[120:121], off offset:1200
	ds_read_b64 v[88:89], v122 offset:48
	ds_read_b64 v[90:91], v122 offset:560
	ds_read_b64 v[92:93], v122 offset:1072
	ds_read_b64 v[94:95], v122 offset:1584
	ds_read_b64 v[96:97], v122 offset:2096
	ds_read_b64 v[98:99], v122 offset:2608
	ds_read_b64 v[100:101], v122 offset:3120
	ds_read_b64 v[102:103], v122 offset:3632
	v_lshl_add_u64 v[120:121], v[120:121], 0, s[10:11]
	s_waitcnt vmcnt(10) lgkmcnt(8)
	v_pk_fma_f32 v[4:5], v[104:105], v[80:81], v[4:5] op_sel_hi:[0,1,1]
	v_pk_fma_f32 v[6:7], v[104:105], v[82:83], v[6:7] op_sel_hi:[0,1,1]
	v_pk_fma_f32 v[8:9], v[106:107], v[80:81], v[8:9] op_sel_hi:[0,1,1]
	v_pk_fma_f32 v[10:11], v[106:107], v[82:83], v[10:11] op_sel_hi:[0,1,1]
	v_pk_fma_f32 v[12:13], v[108:109], v[80:81], v[12:13] op_sel_hi:[0,1,1]
	v_pk_fma_f32 v[14:15], v[108:109], v[82:83], v[14:15] op_sel_hi:[0,1,1]
	v_pk_fma_f32 v[16:17], v[110:111], v[80:81], v[16:17] op_sel_hi:[0,1,1]
	v_pk_fma_f32 v[18:19], v[110:111], v[82:83], v[18:19] op_sel_hi:[0,1,1]
	v_pk_fma_f32 v[20:21], v[112:113], v[80:81], v[20:21] op_sel_hi:[0,1,1]
	v_pk_fma_f32 v[22:23], v[112:113], v[82:83], v[22:23] op_sel_hi:[0,1,1]
	v_pk_fma_f32 v[24:25], v[114:115], v[80:81], v[24:25] op_sel_hi:[0,1,1]
	v_pk_fma_f32 v[26:27], v[114:115], v[82:83], v[26:27] op_sel_hi:[0,1,1]
	v_pk_fma_f32 v[28:29], v[116:117], v[80:81], v[28:29] op_sel_hi:[0,1,1]
	v_pk_fma_f32 v[30:31], v[116:117], v[82:83], v[30:31] op_sel_hi:[0,1,1]
	v_pk_fma_f32 v[32:33], v[118:119], v[80:81], v[32:33] op_sel_hi:[0,1,1]
	v_pk_fma_f32 v[34:35], v[118:119], v[82:83], v[34:35] op_sel_hi:[0,1,1]
	v_pk_fma_f32 v[4:5], v[104:105], v[84:85], v[4:5] op_sel:[1,0,0]
	v_pk_fma_f32 v[6:7], v[104:105], v[86:87], v[6:7] op_sel:[1,0,0]
	v_pk_fma_f32 v[8:9], v[106:107], v[84:85], v[8:9] op_sel:[1,0,0]
	v_pk_fma_f32 v[10:11], v[106:107], v[86:87], v[10:11] op_sel:[1,0,0]
	v_pk_fma_f32 v[12:13], v[108:109], v[84:85], v[12:13] op_sel:[1,0,0]
	v_pk_fma_f32 v[14:15], v[108:109], v[86:87], v[14:15] op_sel:[1,0,0]
	v_pk_fma_f32 v[16:17], v[110:111], v[84:85], v[16:17] op_sel:[1,0,0]
	v_pk_fma_f32 v[18:19], v[110:111], v[86:87], v[18:19] op_sel:[1,0,0]
	v_pk_fma_f32 v[20:21], v[112:113], v[84:85], v[20:21] op_sel:[1,0,0]
	v_pk_fma_f32 v[22:23], v[112:113], v[86:87], v[22:23] op_sel:[1,0,0]
	v_pk_fma_f32 v[24:25], v[114:115], v[84:85], v[24:25] op_sel:[1,0,0]
	v_pk_fma_f32 v[26:27], v[114:115], v[86:87], v[26:27] op_sel:[1,0,0]
	v_pk_fma_f32 v[28:29], v[116:117], v[84:85], v[28:29] op_sel:[1,0,0]
	v_pk_fma_f32 v[30:31], v[116:117], v[86:87], v[30:31] op_sel:[1,0,0]
	v_pk_fma_f32 v[32:33], v[118:119], v[84:85], v[32:33] op_sel:[1,0,0]
	v_pk_fma_f32 v[34:35], v[118:119], v[86:87], v[34:35] op_sel:[1,0,0]
	global_load_dwordx4 v[80:83], v[120:121], off
	global_load_dwordx4 v[84:87], v[120:121], off offset:1200
	ds_read_b64 v[104:105], v122 offset:56
	ds_read_b64 v[106:107], v122 offset:568
	ds_read_b64 v[108:109], v122 offset:1080
	ds_read_b64 v[110:111], v122 offset:1592
	ds_read_b64 v[112:113], v122 offset:2104
	ds_read_b64 v[114:115], v122 offset:2616
	ds_read_b64 v[116:117], v122 offset:3128
	ds_read_b64 v[118:119], v122 offset:3640
	v_lshl_add_u64 v[120:121], v[120:121], 0, s[10:11]
	s_waitcnt vmcnt(10) lgkmcnt(8)
	v_pk_fma_f32 v[4:5], v[88:89], v[36:37], v[4:5] op_sel_hi:[0,1,1]
	v_pk_fma_f32 v[6:7], v[88:89], v[38:39], v[6:7] op_sel_hi:[0,1,1]
	v_pk_fma_f32 v[8:9], v[90:91], v[36:37], v[8:9] op_sel_hi:[0,1,1]
	v_pk_fma_f32 v[10:11], v[90:91], v[38:39], v[10:11] op_sel_hi:[0,1,1]
	v_pk_fma_f32 v[12:13], v[92:93], v[36:37], v[12:13] op_sel_hi:[0,1,1]
	v_pk_fma_f32 v[14:15], v[92:93], v[38:39], v[14:15] op_sel_hi:[0,1,1]
	v_pk_fma_f32 v[16:17], v[94:95], v[36:37], v[16:17] op_sel_hi:[0,1,1]
	v_pk_fma_f32 v[18:19], v[94:95], v[38:39], v[18:19] op_sel_hi:[0,1,1]
	v_pk_fma_f32 v[20:21], v[96:97], v[36:37], v[20:21] op_sel_hi:[0,1,1]
	v_pk_fma_f32 v[22:23], v[96:97], v[38:39], v[22:23] op_sel_hi:[0,1,1]
	v_pk_fma_f32 v[24:25], v[98:99], v[36:37], v[24:25] op_sel_hi:[0,1,1]
	v_pk_fma_f32 v[26:27], v[98:99], v[38:39], v[26:27] op_sel_hi:[0,1,1]
	v_pk_fma_f32 v[28:29], v[100:101], v[36:37], v[28:29] op_sel_hi:[0,1,1]
	v_pk_fma_f32 v[30:31], v[100:101], v[38:39], v[30:31] op_sel_hi:[0,1,1]
	v_pk_fma_f32 v[32:33], v[102:103], v[36:37], v[32:33] op_sel_hi:[0,1,1]
	v_pk_fma_f32 v[34:35], v[102:103], v[38:39], v[34:35] op_sel_hi:[0,1,1]
	v_pk_fma_f32 v[4:5], v[88:89], v[40:41], v[4:5] op_sel:[1,0,0]
	v_pk_fma_f32 v[6:7], v[88:89], v[42:43], v[6:7] op_sel:[1,0,0]
	v_pk_fma_f32 v[8:9], v[90:91], v[40:41], v[8:9] op_sel:[1,0,0]
	v_pk_fma_f32 v[10:11], v[90:91], v[42:43], v[10:11] op_sel:[1,0,0]
	v_pk_fma_f32 v[12:13], v[92:93], v[40:41], v[12:13] op_sel:[1,0,0]
	v_pk_fma_f32 v[14:15], v[92:93], v[42:43], v[14:15] op_sel:[1,0,0]
	v_pk_fma_f32 v[16:17], v[94:95], v[40:41], v[16:17] op_sel:[1,0,0]
	v_pk_fma_f32 v[18:19], v[94:95], v[42:43], v[18:19] op_sel:[1,0,0]
	v_pk_fma_f32 v[20:21], v[96:97], v[40:41], v[20:21] op_sel:[1,0,0]
	v_pk_fma_f32 v[22:23], v[96:97], v[42:43], v[22:23] op_sel:[1,0,0]
	v_pk_fma_f32 v[24:25], v[98:99], v[40:41], v[24:25] op_sel:[1,0,0]
	v_pk_fma_f32 v[26:27], v[98:99], v[42:43], v[26:27] op_sel:[1,0,0]
	v_pk_fma_f32 v[28:29], v[100:101], v[40:41], v[28:29] op_sel:[1,0,0]
	v_pk_fma_f32 v[30:31], v[100:101], v[42:43], v[30:31] op_sel:[1,0,0]
	v_pk_fma_f32 v[32:33], v[102:103], v[40:41], v[32:33] op_sel:[1,0,0]
	v_pk_fma_f32 v[34:35], v[102:103], v[42:43], v[34:35] op_sel:[1,0,0]
	global_load_dwordx4 v[36:39], v[120:121], off
	global_load_dwordx4 v[40:43], v[120:121], off offset:1200
	ds_read_b64 v[88:89], v122 offset:64
	ds_read_b64 v[90:91], v122 offset:576
	ds_read_b64 v[92:93], v122 offset:1088
	ds_read_b64 v[94:95], v122 offset:1600
	ds_read_b64 v[96:97], v122 offset:2112
	ds_read_b64 v[98:99], v122 offset:2624
	ds_read_b64 v[100:101], v122 offset:3136
	ds_read_b64 v[102:103], v122 offset:3648
	v_lshl_add_u64 v[120:121], v[120:121], 0, s[10:11]
	s_waitcnt vmcnt(10) lgkmcnt(8)
	v_pk_fma_f32 v[4:5], v[104:105], v[44:45], v[4:5] op_sel_hi:[0,1,1]
	v_pk_fma_f32 v[6:7], v[104:105], v[46:47], v[6:7] op_sel_hi:[0,1,1]
	v_pk_fma_f32 v[8:9], v[106:107], v[44:45], v[8:9] op_sel_hi:[0,1,1]
	v_pk_fma_f32 v[10:11], v[106:107], v[46:47], v[10:11] op_sel_hi:[0,1,1]
	v_pk_fma_f32 v[12:13], v[108:109], v[44:45], v[12:13] op_sel_hi:[0,1,1]
	v_pk_fma_f32 v[14:15], v[108:109], v[46:47], v[14:15] op_sel_hi:[0,1,1]
	v_pk_fma_f32 v[16:17], v[110:111], v[44:45], v[16:17] op_sel_hi:[0,1,1]
	v_pk_fma_f32 v[18:19], v[110:111], v[46:47], v[18:19] op_sel_hi:[0,1,1]
	v_pk_fma_f32 v[20:21], v[112:113], v[44:45], v[20:21] op_sel_hi:[0,1,1]
	v_pk_fma_f32 v[22:23], v[112:113], v[46:47], v[22:23] op_sel_hi:[0,1,1]
	v_pk_fma_f32 v[24:25], v[114:115], v[44:45], v[24:25] op_sel_hi:[0,1,1]
	v_pk_fma_f32 v[26:27], v[114:115], v[46:47], v[26:27] op_sel_hi:[0,1,1]
	v_pk_fma_f32 v[28:29], v[116:117], v[44:45], v[28:29] op_sel_hi:[0,1,1]
	v_pk_fma_f32 v[30:31], v[116:117], v[46:47], v[30:31] op_sel_hi:[0,1,1]
	v_pk_fma_f32 v[32:33], v[118:119], v[44:45], v[32:33] op_sel_hi:[0,1,1]
	v_pk_fma_f32 v[34:35], v[118:119], v[46:47], v[34:35] op_sel_hi:[0,1,1]
	v_pk_fma_f32 v[4:5], v[104:105], v[48:49], v[4:5] op_sel:[1,0,0]
	v_pk_fma_f32 v[6:7], v[104:105], v[50:51], v[6:7] op_sel:[1,0,0]
	v_pk_fma_f32 v[8:9], v[106:107], v[48:49], v[8:9] op_sel:[1,0,0]
	v_pk_fma_f32 v[10:11], v[106:107], v[50:51], v[10:11] op_sel:[1,0,0]
	v_pk_fma_f32 v[12:13], v[108:109], v[48:49], v[12:13] op_sel:[1,0,0]
	v_pk_fma_f32 v[14:15], v[108:109], v[50:51], v[14:15] op_sel:[1,0,0]
	v_pk_fma_f32 v[16:17], v[110:111], v[48:49], v[16:17] op_sel:[1,0,0]
	v_pk_fma_f32 v[18:19], v[110:111], v[50:51], v[18:19] op_sel:[1,0,0]
	v_pk_fma_f32 v[20:21], v[112:113], v[48:49], v[20:21] op_sel:[1,0,0]
	v_pk_fma_f32 v[22:23], v[112:113], v[50:51], v[22:23] op_sel:[1,0,0]
	v_pk_fma_f32 v[24:25], v[114:115], v[48:49], v[24:25] op_sel:[1,0,0]
	v_pk_fma_f32 v[26:27], v[114:115], v[50:51], v[26:27] op_sel:[1,0,0]
	v_pk_fma_f32 v[28:29], v[116:117], v[48:49], v[28:29] op_sel:[1,0,0]
	v_pk_fma_f32 v[30:31], v[116:117], v[50:51], v[30:31] op_sel:[1,0,0]
	v_pk_fma_f32 v[32:33], v[118:119], v[48:49], v[32:33] op_sel:[1,0,0]
	v_pk_fma_f32 v[34:35], v[118:119], v[50:51], v[34:35] op_sel:[1,0,0]
	global_load_dwordx4 v[44:47], v[120:121], off
	global_load_dwordx4 v[48:51], v[120:121], off offset:1200
	ds_read_b64 v[104:105], v122 offset:72
	ds_read_b64 v[106:107], v122 offset:584
	ds_read_b64 v[108:109], v122 offset:1096
	ds_read_b64 v[110:111], v122 offset:1608
	ds_read_b64 v[112:113], v122 offset:2120
	ds_read_b64 v[114:115], v122 offset:2632
	ds_read_b64 v[116:117], v122 offset:3144
	ds_read_b64 v[118:119], v122 offset:3656
	v_lshl_add_u64 v[120:121], v[120:121], 0, s[10:11]
	s_waitcnt vmcnt(10) lgkmcnt(8)
	v_pk_fma_f32 v[4:5], v[88:89], v[52:53], v[4:5] op_sel_hi:[0,1,1]
	v_pk_fma_f32 v[6:7], v[88:89], v[54:55], v[6:7] op_sel_hi:[0,1,1]
	v_pk_fma_f32 v[8:9], v[90:91], v[52:53], v[8:9] op_sel_hi:[0,1,1]
	v_pk_fma_f32 v[10:11], v[90:91], v[54:55], v[10:11] op_sel_hi:[0,1,1]
	v_pk_fma_f32 v[12:13], v[92:93], v[52:53], v[12:13] op_sel_hi:[0,1,1]
	v_pk_fma_f32 v[14:15], v[92:93], v[54:55], v[14:15] op_sel_hi:[0,1,1]
	v_pk_fma_f32 v[16:17], v[94:95], v[52:53], v[16:17] op_sel_hi:[0,1,1]
	v_pk_fma_f32 v[18:19], v[94:95], v[54:55], v[18:19] op_sel_hi:[0,1,1]
	v_pk_fma_f32 v[20:21], v[96:97], v[52:53], v[20:21] op_sel_hi:[0,1,1]
	v_pk_fma_f32 v[22:23], v[96:97], v[54:55], v[22:23] op_sel_hi:[0,1,1]
	v_pk_fma_f32 v[24:25], v[98:99], v[52:53], v[24:25] op_sel_hi:[0,1,1]
	v_pk_fma_f32 v[26:27], v[98:99], v[54:55], v[26:27] op_sel_hi:[0,1,1]
	v_pk_fma_f32 v[28:29], v[100:101], v[52:53], v[28:29] op_sel_hi:[0,1,1]
	v_pk_fma_f32 v[30:31], v[100:101], v[54:55], v[30:31] op_sel_hi:[0,1,1]
	v_pk_fma_f32 v[32:33], v[102:103], v[52:53], v[32:33] op_sel_hi:[0,1,1]
	v_pk_fma_f32 v[34:35], v[102:103], v[54:55], v[34:35] op_sel_hi:[0,1,1]
	v_pk_fma_f32 v[4:5], v[88:89], v[56:57], v[4:5] op_sel:[1,0,0]
	v_pk_fma_f32 v[6:7], v[88:89], v[58:59], v[6:7] op_sel:[1,0,0]
	v_pk_fma_f32 v[8:9], v[90:91], v[56:57], v[8:9] op_sel:[1,0,0]
	v_pk_fma_f32 v[10:11], v[90:91], v[58:59], v[10:11] op_sel:[1,0,0]
	v_pk_fma_f32 v[12:13], v[92:93], v[56:57], v[12:13] op_sel:[1,0,0]
	v_pk_fma_f32 v[14:15], v[92:93], v[58:59], v[14:15] op_sel:[1,0,0]
	v_pk_fma_f32 v[16:17], v[94:95], v[56:57], v[16:17] op_sel:[1,0,0]
	v_pk_fma_f32 v[18:19], v[94:95], v[58:59], v[18:19] op_sel:[1,0,0]
	v_pk_fma_f32 v[20:21], v[96:97], v[56:57], v[20:21] op_sel:[1,0,0]
	v_pk_fma_f32 v[22:23], v[96:97], v[58:59], v[22:23] op_sel:[1,0,0]
	v_pk_fma_f32 v[24:25], v[98:99], v[56:57], v[24:25] op_sel:[1,0,0]
	v_pk_fma_f32 v[26:27], v[98:99], v[58:59], v[26:27] op_sel:[1,0,0]
	v_pk_fma_f32 v[28:29], v[100:101], v[56:57], v[28:29] op_sel:[1,0,0]
	v_pk_fma_f32 v[30:31], v[100:101], v[58:59], v[30:31] op_sel:[1,0,0]
	v_pk_fma_f32 v[32:33], v[102:103], v[56:57], v[32:33] op_sel:[1,0,0]
	v_pk_fma_f32 v[34:35], v[102:103], v[58:59], v[34:35] op_sel:[1,0,0]
	global_load_dwordx4 v[52:55], v[120:121], off
	global_load_dwordx4 v[56:59], v[120:121], off offset:1200
	ds_read_b64 v[88:89], v122 offset:80
	ds_read_b64 v[90:91], v122 offset:592
	ds_read_b64 v[92:93], v122 offset:1104
	ds_read_b64 v[94:95], v122 offset:1616
	ds_read_b64 v[96:97], v122 offset:2128
	ds_read_b64 v[98:99], v122 offset:2640
	ds_read_b64 v[100:101], v122 offset:3152
	ds_read_b64 v[102:103], v122 offset:3664
	v_lshl_add_u64 v[120:121], v[120:121], 0, s[10:11]
	s_waitcnt vmcnt(10) lgkmcnt(8)
	v_pk_fma_f32 v[4:5], v[104:105], v[60:61], v[4:5] op_sel_hi:[0,1,1]
	v_pk_fma_f32 v[6:7], v[104:105], v[62:63], v[6:7] op_sel_hi:[0,1,1]
	v_pk_fma_f32 v[8:9], v[106:107], v[60:61], v[8:9] op_sel_hi:[0,1,1]
	v_pk_fma_f32 v[10:11], v[106:107], v[62:63], v[10:11] op_sel_hi:[0,1,1]
	v_pk_fma_f32 v[12:13], v[108:109], v[60:61], v[12:13] op_sel_hi:[0,1,1]
	v_pk_fma_f32 v[14:15], v[108:109], v[62:63], v[14:15] op_sel_hi:[0,1,1]
	v_pk_fma_f32 v[16:17], v[110:111], v[60:61], v[16:17] op_sel_hi:[0,1,1]
	v_pk_fma_f32 v[18:19], v[110:111], v[62:63], v[18:19] op_sel_hi:[0,1,1]
	v_pk_fma_f32 v[20:21], v[112:113], v[60:61], v[20:21] op_sel_hi:[0,1,1]
	v_pk_fma_f32 v[22:23], v[112:113], v[62:63], v[22:23] op_sel_hi:[0,1,1]
	v_pk_fma_f32 v[24:25], v[114:115], v[60:61], v[24:25] op_sel_hi:[0,1,1]
	v_pk_fma_f32 v[26:27], v[114:115], v[62:63], v[26:27] op_sel_hi:[0,1,1]
	v_pk_fma_f32 v[28:29], v[116:117], v[60:61], v[28:29] op_sel_hi:[0,1,1]
	v_pk_fma_f32 v[30:31], v[116:117], v[62:63], v[30:31] op_sel_hi:[0,1,1]
	v_pk_fma_f32 v[32:33], v[118:119], v[60:61], v[32:33] op_sel_hi:[0,1,1]
	v_pk_fma_f32 v[34:35], v[118:119], v[62:63], v[34:35] op_sel_hi:[0,1,1]
	v_pk_fma_f32 v[4:5], v[104:105], v[64:65], v[4:5] op_sel:[1,0,0]
	v_pk_fma_f32 v[6:7], v[104:105], v[66:67], v[6:7] op_sel:[1,0,0]
	v_pk_fma_f32 v[8:9], v[106:107], v[64:65], v[8:9] op_sel:[1,0,0]
	v_pk_fma_f32 v[10:11], v[106:107], v[66:67], v[10:11] op_sel:[1,0,0]
	v_pk_fma_f32 v[12:13], v[108:109], v[64:65], v[12:13] op_sel:[1,0,0]
	v_pk_fma_f32 v[14:15], v[108:109], v[66:67], v[14:15] op_sel:[1,0,0]
	v_pk_fma_f32 v[16:17], v[110:111], v[64:65], v[16:17] op_sel:[1,0,0]
	v_pk_fma_f32 v[18:19], v[110:111], v[66:67], v[18:19] op_sel:[1,0,0]
	v_pk_fma_f32 v[20:21], v[112:113], v[64:65], v[20:21] op_sel:[1,0,0]
	v_pk_fma_f32 v[22:23], v[112:113], v[66:67], v[22:23] op_sel:[1,0,0]
	v_pk_fma_f32 v[24:25], v[114:115], v[64:65], v[24:25] op_sel:[1,0,0]
	v_pk_fma_f32 v[26:27], v[114:115], v[66:67], v[26:27] op_sel:[1,0,0]
	v_pk_fma_f32 v[28:29], v[116:117], v[64:65], v[28:29] op_sel:[1,0,0]
	v_pk_fma_f32 v[30:31], v[116:117], v[66:67], v[30:31] op_sel:[1,0,0]
	v_pk_fma_f32 v[32:33], v[118:119], v[64:65], v[32:33] op_sel:[1,0,0]
	v_pk_fma_f32 v[34:35], v[118:119], v[66:67], v[34:35] op_sel:[1,0,0]
	global_load_dwordx4 v[60:63], v[120:121], off
	global_load_dwordx4 v[64:67], v[120:121], off offset:1200
	ds_read_b64 v[104:105], v122 offset:88
	ds_read_b64 v[106:107], v122 offset:600
	ds_read_b64 v[108:109], v122 offset:1112
	ds_read_b64 v[110:111], v122 offset:1624
	ds_read_b64 v[112:113], v122 offset:2136
	ds_read_b64 v[114:115], v122 offset:2648
	ds_read_b64 v[116:117], v122 offset:3160
	ds_read_b64 v[118:119], v122 offset:3672
	v_lshl_add_u64 v[120:121], v[120:121], 0, s[10:11]
	s_waitcnt vmcnt(10) lgkmcnt(8)
	v_pk_fma_f32 v[4:5], v[88:89], v[72:73], v[4:5] op_sel_hi:[0,1,1]
	v_pk_fma_f32 v[6:7], v[88:89], v[74:75], v[6:7] op_sel_hi:[0,1,1]
	v_pk_fma_f32 v[8:9], v[90:91], v[72:73], v[8:9] op_sel_hi:[0,1,1]
	v_pk_fma_f32 v[10:11], v[90:91], v[74:75], v[10:11] op_sel_hi:[0,1,1]
	v_pk_fma_f32 v[12:13], v[92:93], v[72:73], v[12:13] op_sel_hi:[0,1,1]
	v_pk_fma_f32 v[14:15], v[92:93], v[74:75], v[14:15] op_sel_hi:[0,1,1]
	v_pk_fma_f32 v[16:17], v[94:95], v[72:73], v[16:17] op_sel_hi:[0,1,1]
	v_pk_fma_f32 v[18:19], v[94:95], v[74:75], v[18:19] op_sel_hi:[0,1,1]
	v_pk_fma_f32 v[20:21], v[96:97], v[72:73], v[20:21] op_sel_hi:[0,1,1]
	v_pk_fma_f32 v[22:23], v[96:97], v[74:75], v[22:23] op_sel_hi:[0,1,1]
	v_pk_fma_f32 v[24:25], v[98:99], v[72:73], v[24:25] op_sel_hi:[0,1,1]
	v_pk_fma_f32 v[26:27], v[98:99], v[74:75], v[26:27] op_sel_hi:[0,1,1]
	v_pk_fma_f32 v[28:29], v[100:101], v[72:73], v[28:29] op_sel_hi:[0,1,1]
	v_pk_fma_f32 v[30:31], v[100:101], v[74:75], v[30:31] op_sel_hi:[0,1,1]
	v_pk_fma_f32 v[32:33], v[102:103], v[72:73], v[32:33] op_sel_hi:[0,1,1]
	v_pk_fma_f32 v[34:35], v[102:103], v[74:75], v[34:35] op_sel_hi:[0,1,1]
	v_pk_fma_f32 v[4:5], v[88:89], v[76:77], v[4:5] op_sel:[1,0,0]
	v_pk_fma_f32 v[6:7], v[88:89], v[78:79], v[6:7] op_sel:[1,0,0]
	v_pk_fma_f32 v[8:9], v[90:91], v[76:77], v[8:9] op_sel:[1,0,0]
	v_pk_fma_f32 v[10:11], v[90:91], v[78:79], v[10:11] op_sel:[1,0,0]
	v_pk_fma_f32 v[12:13], v[92:93], v[76:77], v[12:13] op_sel:[1,0,0]
	v_pk_fma_f32 v[14:15], v[92:93], v[78:79], v[14:15] op_sel:[1,0,0]
	v_pk_fma_f32 v[16:17], v[94:95], v[76:77], v[16:17] op_sel:[1,0,0]
	v_pk_fma_f32 v[18:19], v[94:95], v[78:79], v[18:19] op_sel:[1,0,0]
	v_pk_fma_f32 v[20:21], v[96:97], v[76:77], v[20:21] op_sel:[1,0,0]
	v_pk_fma_f32 v[22:23], v[96:97], v[78:79], v[22:23] op_sel:[1,0,0]
	v_pk_fma_f32 v[24:25], v[98:99], v[76:77], v[24:25] op_sel:[1,0,0]
	v_pk_fma_f32 v[26:27], v[98:99], v[78:79], v[26:27] op_sel:[1,0,0]
	v_pk_fma_f32 v[28:29], v[100:101], v[76:77], v[28:29] op_sel:[1,0,0]
	v_pk_fma_f32 v[30:31], v[100:101], v[78:79], v[30:31] op_sel:[1,0,0]
	v_pk_fma_f32 v[32:33], v[102:103], v[76:77], v[32:33] op_sel:[1,0,0]
	v_pk_fma_f32 v[34:35], v[102:103], v[78:79], v[34:35] op_sel:[1,0,0]
	ds_read_b64 v[88:89], v122 offset:96
	ds_read_b64 v[90:91], v122 offset:608
	ds_read_b64 v[92:93], v122 offset:1120
	ds_read_b64 v[94:95], v122 offset:1632
	ds_read_b64 v[96:97], v122 offset:2144
	ds_read_b64 v[98:99], v122 offset:2656
	ds_read_b64 v[100:101], v122 offset:3168
	ds_read_b64 v[102:103], v122 offset:3680
	s_waitcnt vmcnt(8) lgkmcnt(8)
	v_pk_fma_f32 v[4:5], v[104:105], v[80:81], v[4:5] op_sel_hi:[0,1,1]
	v_pk_fma_f32 v[6:7], v[104:105], v[82:83], v[6:7] op_sel_hi:[0,1,1]
	v_pk_fma_f32 v[8:9], v[106:107], v[80:81], v[8:9] op_sel_hi:[0,1,1]
	v_pk_fma_f32 v[10:11], v[106:107], v[82:83], v[10:11] op_sel_hi:[0,1,1]
	v_pk_fma_f32 v[12:13], v[108:109], v[80:81], v[12:13] op_sel_hi:[0,1,1]
	v_pk_fma_f32 v[14:15], v[108:109], v[82:83], v[14:15] op_sel_hi:[0,1,1]
	v_pk_fma_f32 v[16:17], v[110:111], v[80:81], v[16:17] op_sel_hi:[0,1,1]
	v_pk_fma_f32 v[18:19], v[110:111], v[82:83], v[18:19] op_sel_hi:[0,1,1]
	v_pk_fma_f32 v[20:21], v[112:113], v[80:81], v[20:21] op_sel_hi:[0,1,1]
	v_pk_fma_f32 v[22:23], v[112:113], v[82:83], v[22:23] op_sel_hi:[0,1,1]
	v_pk_fma_f32 v[24:25], v[114:115], v[80:81], v[24:25] op_sel_hi:[0,1,1]
	v_pk_fma_f32 v[26:27], v[114:115], v[82:83], v[26:27] op_sel_hi:[0,1,1]
	v_pk_fma_f32 v[28:29], v[116:117], v[80:81], v[28:29] op_sel_hi:[0,1,1]
	v_pk_fma_f32 v[30:31], v[116:117], v[82:83], v[30:31] op_sel_hi:[0,1,1]
	v_pk_fma_f32 v[32:33], v[118:119], v[80:81], v[32:33] op_sel_hi:[0,1,1]
	v_pk_fma_f32 v[34:35], v[118:119], v[82:83], v[34:35] op_sel_hi:[0,1,1]
	v_pk_fma_f32 v[4:5], v[104:105], v[84:85], v[4:5] op_sel:[1,0,0]
	v_pk_fma_f32 v[6:7], v[104:105], v[86:87], v[6:7] op_sel:[1,0,0]
	v_pk_fma_f32 v[8:9], v[106:107], v[84:85], v[8:9] op_sel:[1,0,0]
	v_pk_fma_f32 v[10:11], v[106:107], v[86:87], v[10:11] op_sel:[1,0,0]
	v_pk_fma_f32 v[12:13], v[108:109], v[84:85], v[12:13] op_sel:[1,0,0]
	v_pk_fma_f32 v[14:15], v[108:109], v[86:87], v[14:15] op_sel:[1,0,0]
	v_pk_fma_f32 v[16:17], v[110:111], v[84:85], v[16:17] op_sel:[1,0,0]
	v_pk_fma_f32 v[18:19], v[110:111], v[86:87], v[18:19] op_sel:[1,0,0]
	v_pk_fma_f32 v[20:21], v[112:113], v[84:85], v[20:21] op_sel:[1,0,0]
	v_pk_fma_f32 v[22:23], v[112:113], v[86:87], v[22:23] op_sel:[1,0,0]
	v_pk_fma_f32 v[24:25], v[114:115], v[84:85], v[24:25] op_sel:[1,0,0]
	v_pk_fma_f32 v[26:27], v[114:115], v[86:87], v[26:27] op_sel:[1,0,0]
	v_pk_fma_f32 v[28:29], v[116:117], v[84:85], v[28:29] op_sel:[1,0,0]
	v_pk_fma_f32 v[30:31], v[116:117], v[86:87], v[30:31] op_sel:[1,0,0]
	v_pk_fma_f32 v[32:33], v[118:119], v[84:85], v[32:33] op_sel:[1,0,0]
	v_pk_fma_f32 v[34:35], v[118:119], v[86:87], v[34:35] op_sel:[1,0,0]
	ds_read_b64 v[104:105], v122 offset:104
	ds_read_b64 v[106:107], v122 offset:616
	ds_read_b64 v[108:109], v122 offset:1128
	ds_read_b64 v[110:111], v122 offset:1640
	ds_read_b64 v[112:113], v122 offset:2152
	ds_read_b64 v[114:115], v122 offset:2664
	ds_read_b64 v[116:117], v122 offset:3176
	ds_read_b64 v[118:119], v122 offset:3688
	s_waitcnt vmcnt(6) lgkmcnt(8)
	v_pk_fma_f32 v[4:5], v[88:89], v[36:37], v[4:5] op_sel_hi:[0,1,1]
	v_pk_fma_f32 v[6:7], v[88:89], v[38:39], v[6:7] op_sel_hi:[0,1,1]
	v_pk_fma_f32 v[8:9], v[90:91], v[36:37], v[8:9] op_sel_hi:[0,1,1]
	v_pk_fma_f32 v[10:11], v[90:91], v[38:39], v[10:11] op_sel_hi:[0,1,1]
	v_pk_fma_f32 v[12:13], v[92:93], v[36:37], v[12:13] op_sel_hi:[0,1,1]
	v_pk_fma_f32 v[14:15], v[92:93], v[38:39], v[14:15] op_sel_hi:[0,1,1]
	v_pk_fma_f32 v[16:17], v[94:95], v[36:37], v[16:17] op_sel_hi:[0,1,1]
	v_pk_fma_f32 v[18:19], v[94:95], v[38:39], v[18:19] op_sel_hi:[0,1,1]
	v_pk_fma_f32 v[20:21], v[96:97], v[36:37], v[20:21] op_sel_hi:[0,1,1]
	v_pk_fma_f32 v[22:23], v[96:97], v[38:39], v[22:23] op_sel_hi:[0,1,1]
	v_pk_fma_f32 v[24:25], v[98:99], v[36:37], v[24:25] op_sel_hi:[0,1,1]
	v_pk_fma_f32 v[26:27], v[98:99], v[38:39], v[26:27] op_sel_hi:[0,1,1]
	v_pk_fma_f32 v[28:29], v[100:101], v[36:37], v[28:29] op_sel_hi:[0,1,1]
	v_pk_fma_f32 v[30:31], v[100:101], v[38:39], v[30:31] op_sel_hi:[0,1,1]
	v_pk_fma_f32 v[32:33], v[102:103], v[36:37], v[32:33] op_sel_hi:[0,1,1]
	v_pk_fma_f32 v[34:35], v[102:103], v[38:39], v[34:35] op_sel_hi:[0,1,1]
	v_pk_fma_f32 v[4:5], v[88:89], v[40:41], v[4:5] op_sel:[1,0,0]
	v_pk_fma_f32 v[6:7], v[88:89], v[42:43], v[6:7] op_sel:[1,0,0]
	v_pk_fma_f32 v[8:9], v[90:91], v[40:41], v[8:9] op_sel:[1,0,0]
	v_pk_fma_f32 v[10:11], v[90:91], v[42:43], v[10:11] op_sel:[1,0,0]
	v_pk_fma_f32 v[12:13], v[92:93], v[40:41], v[12:13] op_sel:[1,0,0]
	v_pk_fma_f32 v[14:15], v[92:93], v[42:43], v[14:15] op_sel:[1,0,0]
	v_pk_fma_f32 v[16:17], v[94:95], v[40:41], v[16:17] op_sel:[1,0,0]
	v_pk_fma_f32 v[18:19], v[94:95], v[42:43], v[18:19] op_sel:[1,0,0]
	v_pk_fma_f32 v[20:21], v[96:97], v[40:41], v[20:21] op_sel:[1,0,0]
	v_pk_fma_f32 v[22:23], v[96:97], v[42:43], v[22:23] op_sel:[1,0,0]
	v_pk_fma_f32 v[24:25], v[98:99], v[40:41], v[24:25] op_sel:[1,0,0]
	v_pk_fma_f32 v[26:27], v[98:99], v[42:43], v[26:27] op_sel:[1,0,0]
	v_pk_fma_f32 v[28:29], v[100:101], v[40:41], v[28:29] op_sel:[1,0,0]
	v_pk_fma_f32 v[30:31], v[100:101], v[42:43], v[30:31] op_sel:[1,0,0]
	v_pk_fma_f32 v[32:33], v[102:103], v[40:41], v[32:33] op_sel:[1,0,0]
	v_pk_fma_f32 v[34:35], v[102:103], v[42:43], v[34:35] op_sel:[1,0,0]
	ds_read_b64 v[88:89], v122 offset:112
	ds_read_b64 v[90:91], v122 offset:624
	ds_read_b64 v[92:93], v122 offset:1136
	ds_read_b64 v[94:95], v122 offset:1648
	ds_read_b64 v[96:97], v122 offset:2160
	ds_read_b64 v[98:99], v122 offset:2672
	ds_read_b64 v[100:101], v122 offset:3184
	ds_read_b64 v[102:103], v122 offset:3696
	s_waitcnt vmcnt(4) lgkmcnt(8)
	v_pk_fma_f32 v[4:5], v[104:105], v[44:45], v[4:5] op_sel_hi:[0,1,1]
	v_pk_fma_f32 v[6:7], v[104:105], v[46:47], v[6:7] op_sel_hi:[0,1,1]
	v_pk_fma_f32 v[8:9], v[106:107], v[44:45], v[8:9] op_sel_hi:[0,1,1]
	v_pk_fma_f32 v[10:11], v[106:107], v[46:47], v[10:11] op_sel_hi:[0,1,1]
	v_pk_fma_f32 v[12:13], v[108:109], v[44:45], v[12:13] op_sel_hi:[0,1,1]
	v_pk_fma_f32 v[14:15], v[108:109], v[46:47], v[14:15] op_sel_hi:[0,1,1]
	v_pk_fma_f32 v[16:17], v[110:111], v[44:45], v[16:17] op_sel_hi:[0,1,1]
	v_pk_fma_f32 v[18:19], v[110:111], v[46:47], v[18:19] op_sel_hi:[0,1,1]
	v_pk_fma_f32 v[20:21], v[112:113], v[44:45], v[20:21] op_sel_hi:[0,1,1]
	v_pk_fma_f32 v[22:23], v[112:113], v[46:47], v[22:23] op_sel_hi:[0,1,1]
	v_pk_fma_f32 v[24:25], v[114:115], v[44:45], v[24:25] op_sel_hi:[0,1,1]
	v_pk_fma_f32 v[26:27], v[114:115], v[46:47], v[26:27] op_sel_hi:[0,1,1]
	v_pk_fma_f32 v[28:29], v[116:117], v[44:45], v[28:29] op_sel_hi:[0,1,1]
	v_pk_fma_f32 v[30:31], v[116:117], v[46:47], v[30:31] op_sel_hi:[0,1,1]
	v_pk_fma_f32 v[32:33], v[118:119], v[44:45], v[32:33] op_sel_hi:[0,1,1]
	v_pk_fma_f32 v[34:35], v[118:119], v[46:47], v[34:35] op_sel_hi:[0,1,1]
	v_pk_fma_f32 v[4:5], v[104:105], v[48:49], v[4:5] op_sel:[1,0,0]
	v_pk_fma_f32 v[6:7], v[104:105], v[50:51], v[6:7] op_sel:[1,0,0]
	v_pk_fma_f32 v[8:9], v[106:107], v[48:49], v[8:9] op_sel:[1,0,0]
	v_pk_fma_f32 v[10:11], v[106:107], v[50:51], v[10:11] op_sel:[1,0,0]
	v_pk_fma_f32 v[12:13], v[108:109], v[48:49], v[12:13] op_sel:[1,0,0]
	v_pk_fma_f32 v[14:15], v[108:109], v[50:51], v[14:15] op_sel:[1,0,0]
	v_pk_fma_f32 v[16:17], v[110:111], v[48:49], v[16:17] op_sel:[1,0,0]
	v_pk_fma_f32 v[18:19], v[110:111], v[50:51], v[18:19] op_sel:[1,0,0]
	v_pk_fma_f32 v[20:21], v[112:113], v[48:49], v[20:21] op_sel:[1,0,0]
	v_pk_fma_f32 v[22:23], v[112:113], v[50:51], v[22:23] op_sel:[1,0,0]
	v_pk_fma_f32 v[24:25], v[114:115], v[48:49], v[24:25] op_sel:[1,0,0]
	v_pk_fma_f32 v[26:27], v[114:115], v[50:51], v[26:27] op_sel:[1,0,0]
	v_pk_fma_f32 v[28:29], v[116:117], v[48:49], v[28:29] op_sel:[1,0,0]
	v_pk_fma_f32 v[30:31], v[116:117], v[50:51], v[30:31] op_sel:[1,0,0]
	v_pk_fma_f32 v[32:33], v[118:119], v[48:49], v[32:33] op_sel:[1,0,0]
	v_pk_fma_f32 v[34:35], v[118:119], v[50:51], v[34:35] op_sel:[1,0,0]
	ds_read_b64 v[104:105], v122 offset:120
	ds_read_b64 v[106:107], v122 offset:632
	ds_read_b64 v[108:109], v122 offset:1144
	ds_read_b64 v[110:111], v122 offset:1656
	ds_read_b64 v[112:113], v122 offset:2168
	ds_read_b64 v[114:115], v122 offset:2680
	ds_read_b64 v[116:117], v122 offset:3192
	ds_read_b64 v[118:119], v122 offset:3704
	s_waitcnt vmcnt(2) lgkmcnt(8)
	v_pk_fma_f32 v[4:5], v[88:89], v[52:53], v[4:5] op_sel_hi:[0,1,1]
	v_pk_fma_f32 v[6:7], v[88:89], v[54:55], v[6:7] op_sel_hi:[0,1,1]
	v_pk_fma_f32 v[8:9], v[90:91], v[52:53], v[8:9] op_sel_hi:[0,1,1]
	v_pk_fma_f32 v[10:11], v[90:91], v[54:55], v[10:11] op_sel_hi:[0,1,1]
	v_pk_fma_f32 v[12:13], v[92:93], v[52:53], v[12:13] op_sel_hi:[0,1,1]
	v_pk_fma_f32 v[14:15], v[92:93], v[54:55], v[14:15] op_sel_hi:[0,1,1]
	v_pk_fma_f32 v[16:17], v[94:95], v[52:53], v[16:17] op_sel_hi:[0,1,1]
	v_pk_fma_f32 v[18:19], v[94:95], v[54:55], v[18:19] op_sel_hi:[0,1,1]
	v_pk_fma_f32 v[20:21], v[96:97], v[52:53], v[20:21] op_sel_hi:[0,1,1]
	v_pk_fma_f32 v[22:23], v[96:97], v[54:55], v[22:23] op_sel_hi:[0,1,1]
	v_pk_fma_f32 v[24:25], v[98:99], v[52:53], v[24:25] op_sel_hi:[0,1,1]
	v_pk_fma_f32 v[26:27], v[98:99], v[54:55], v[26:27] op_sel_hi:[0,1,1]
	v_pk_fma_f32 v[28:29], v[100:101], v[52:53], v[28:29] op_sel_hi:[0,1,1]
	v_pk_fma_f32 v[30:31], v[100:101], v[54:55], v[30:31] op_sel_hi:[0,1,1]
	v_pk_fma_f32 v[32:33], v[102:103], v[52:53], v[32:33] op_sel_hi:[0,1,1]
	v_pk_fma_f32 v[34:35], v[102:103], v[54:55], v[34:35] op_sel_hi:[0,1,1]
	v_pk_fma_f32 v[4:5], v[88:89], v[56:57], v[4:5] op_sel:[1,0,0]
	v_pk_fma_f32 v[6:7], v[88:89], v[58:59], v[6:7] op_sel:[1,0,0]
	v_pk_fma_f32 v[8:9], v[90:91], v[56:57], v[8:9] op_sel:[1,0,0]
	v_pk_fma_f32 v[10:11], v[90:91], v[58:59], v[10:11] op_sel:[1,0,0]
	v_pk_fma_f32 v[12:13], v[92:93], v[56:57], v[12:13] op_sel:[1,0,0]
	v_pk_fma_f32 v[14:15], v[92:93], v[58:59], v[14:15] op_sel:[1,0,0]
	v_pk_fma_f32 v[16:17], v[94:95], v[56:57], v[16:17] op_sel:[1,0,0]
	v_pk_fma_f32 v[18:19], v[94:95], v[58:59], v[18:19] op_sel:[1,0,0]
	v_pk_fma_f32 v[20:21], v[96:97], v[56:57], v[20:21] op_sel:[1,0,0]
	v_pk_fma_f32 v[22:23], v[96:97], v[58:59], v[22:23] op_sel:[1,0,0]
	v_pk_fma_f32 v[24:25], v[98:99], v[56:57], v[24:25] op_sel:[1,0,0]
	v_pk_fma_f32 v[26:27], v[98:99], v[58:59], v[26:27] op_sel:[1,0,0]
	v_pk_fma_f32 v[28:29], v[100:101], v[56:57], v[28:29] op_sel:[1,0,0]
	v_pk_fma_f32 v[30:31], v[100:101], v[58:59], v[30:31] op_sel:[1,0,0]
	v_pk_fma_f32 v[32:33], v[102:103], v[56:57], v[32:33] op_sel:[1,0,0]
	v_pk_fma_f32 v[34:35], v[102:103], v[58:59], v[34:35] op_sel:[1,0,0]
	s_waitcnt vmcnt(0) lgkmcnt(0)
	v_pk_fma_f32 v[4:5], v[104:105], v[60:61], v[4:5] op_sel_hi:[0,1,1]
	v_pk_fma_f32 v[6:7], v[104:105], v[62:63], v[6:7] op_sel_hi:[0,1,1]
	v_pk_fma_f32 v[8:9], v[106:107], v[60:61], v[8:9] op_sel_hi:[0,1,1]
	v_pk_fma_f32 v[10:11], v[106:107], v[62:63], v[10:11] op_sel_hi:[0,1,1]
	v_pk_fma_f32 v[12:13], v[108:109], v[60:61], v[12:13] op_sel_hi:[0,1,1]
	v_pk_fma_f32 v[14:15], v[108:109], v[62:63], v[14:15] op_sel_hi:[0,1,1]
	v_pk_fma_f32 v[16:17], v[110:111], v[60:61], v[16:17] op_sel_hi:[0,1,1]
	v_pk_fma_f32 v[18:19], v[110:111], v[62:63], v[18:19] op_sel_hi:[0,1,1]
	v_pk_fma_f32 v[20:21], v[112:113], v[60:61], v[20:21] op_sel_hi:[0,1,1]
	v_pk_fma_f32 v[22:23], v[112:113], v[62:63], v[22:23] op_sel_hi:[0,1,1]
	v_pk_fma_f32 v[24:25], v[114:115], v[60:61], v[24:25] op_sel_hi:[0,1,1]
	v_pk_fma_f32 v[26:27], v[114:115], v[62:63], v[26:27] op_sel_hi:[0,1,1]
	v_pk_fma_f32 v[28:29], v[116:117], v[60:61], v[28:29] op_sel_hi:[0,1,1]
	v_pk_fma_f32 v[30:31], v[116:117], v[62:63], v[30:31] op_sel_hi:[0,1,1]
	v_pk_fma_f32 v[32:33], v[118:119], v[60:61], v[32:33] op_sel_hi:[0,1,1]
	v_pk_fma_f32 v[34:35], v[118:119], v[62:63], v[34:35] op_sel_hi:[0,1,1]
	v_pk_fma_f32 v[4:5], v[104:105], v[64:65], v[4:5] op_sel:[1,0,0]
	v_pk_fma_f32 v[6:7], v[104:105], v[66:67], v[6:7] op_sel:[1,0,0]
	v_pk_fma_f32 v[8:9], v[106:107], v[64:65], v[8:9] op_sel:[1,0,0]
	v_pk_fma_f32 v[10:11], v[106:107], v[66:67], v[10:11] op_sel:[1,0,0]
	v_pk_fma_f32 v[12:13], v[108:109], v[64:65], v[12:13] op_sel:[1,0,0]
	v_pk_fma_f32 v[14:15], v[108:109], v[66:67], v[14:15] op_sel:[1,0,0]
	v_pk_fma_f32 v[16:17], v[110:111], v[64:65], v[16:17] op_sel:[1,0,0]
	v_pk_fma_f32 v[18:19], v[110:111], v[66:67], v[18:19] op_sel:[1,0,0]
	v_pk_fma_f32 v[20:21], v[112:113], v[64:65], v[20:21] op_sel:[1,0,0]
	v_pk_fma_f32 v[22:23], v[112:113], v[66:67], v[22:23] op_sel:[1,0,0]
	v_pk_fma_f32 v[24:25], v[114:115], v[64:65], v[24:25] op_sel:[1,0,0]
	v_pk_fma_f32 v[26:27], v[114:115], v[66:67], v[26:27] op_sel:[1,0,0]
	v_pk_fma_f32 v[28:29], v[116:117], v[64:65], v[28:29] op_sel:[1,0,0]
	v_pk_fma_f32 v[30:31], v[116:117], v[66:67], v[30:31] op_sel:[1,0,0]
	v_pk_fma_f32 v[32:33], v[118:119], v[64:65], v[32:33] op_sel:[1,0,0]
	v_pk_fma_f32 v[34:35], v[118:119], v[66:67], v[34:35] op_sel:[1,0,0]
	v_mul_u32_u24_e32 v2, 0x4b0, v125
	v_lshl_add_u32 v2, v123, 3, v2
	v_add_u32_e32 v2, 0x4b0, v2
	v_mov_b32_e32 v3, 0
	v_lshl_add_u64 v[100:101], s[12:13], 0, v[2:3]
	v_cmp_ne_u32_e32 vcc, 0, v124
	s_and_saveexec_b64 s[8:9], vcc
	v_add_u32_e32 v1, -1, v124
	v_mul_u32_u24_e32 v1, 0x5dc0, v1
	v_mov_b32_e32 v2, 0x112c0
	v_cmp_eq_u32_e32 vcc, 3, v124
	s_nop 1
	v_cndmask_b32_e32 v1, v1, v2, vcc
	v_add_u32_e32 v127, v126, v1
	ds_write_b128 v127, v[4:7]
	ds_write_b128 v127, v[8:11] offset:1200
	ds_write_b128 v127, v[12:15] offset:2400
	ds_write_b128 v127, v[16:19] offset:3600
	ds_write_b128 v127, v[20:23] offset:4800
	ds_write_b128 v127, v[24:27] offset:6000
	ds_write_b128 v127, v[28:31] offset:7200
	ds_write_b128 v127, v[32:35] offset:8400
	s_branch .Latt3_join
.Latt3_hh:
	v_add_u32_e32 v1, 0xfffffd80, v0
	s_movk_i32 s5, 0x12c
	v_cmp_gt_u32_e32 vcc, s5, v1
	s_and_saveexec_b64 s[6:7], vcc
	v_mul_u32_u24_e32 v124, 0x36a, v1
	v_lshrrev_b32_e32 v124, 16, v124
	v_mul_u32_u24_e32 v2, 0x4b, v124
	v_sub_u32_e32 v123, v1, v2
	v_mov_b32_e32 v125, 0
	s_mul_i32 s8, s22, 0x25800
	s_add_u32 s8, s14, s8
	s_addc_u32 s9, s15, 0
	v_mul_u32_u24_e32 v2, 0x9600, v124
	v_lshl_add_u32 v2, v123, 4, v2
	v_mov_b32_e32 v3, 0
	v_lshl_add_u64 v[120:121], s[8:9], 0, v[2:3]
	v_lshlrev_b32_e32 v122, 7, v124
	v_add_u32_e32 v122, 0xc000, v122
	v_lshlrev_b32_e32 v126, 4, v123
	s_mov_b64 s[10:11], 0x960
	v_mov_b32_e32 v4, 0
	v_mov_b32_e32 v5, 0
	v_mov_b32_e32 v6, 0
	v_mov_b32_e32 v7, 0
	v_mov_b32_e32 v8, 0
	v_mov_b32_e32 v9, 0
	v_mov_b32_e32 v10, 0
	v_mov_b32_e32 v11, 0
	v_mov_b32_e32 v12, 0
	v_mov_b32_e32 v13, 0
	v_mov_b32_e32 v14, 0
	v_mov_b32_e32 v15, 0
	v_mov_b32_e32 v16, 0
	v_mov_b32_e32 v17, 0
	v_mov_b32_e32 v18, 0
	v_mov_b32_e32 v19, 0
	ds_read_b64 v[88:89], v122
	ds_read_b64 v[90:91], v122 offset:512
	ds_read_b64 v[92:93], v122 offset:1024
	ds_read_b64 v[94:95], v122 offset:1536
	global_load_dwordx4 v[36:39], v[120:121], off
	global_load_dwordx4 v[40:43], v[120:121], off offset:1200
	s_nop 0
	v_lshl_add_u64 v[120:121], v[120:121], 0, s[10:11]
	global_load_dwordx4 v[44:47], v[120:121], off
	global_load_dwordx4 v[48:51], v[120:121], off offset:1200
	s_nop 0
	v_lshl_add_u64 v[120:121], v[120:121], 0, s[10:11]
	global_load_dwordx4 v[52:55], v[120:121], off
	global_load_dwordx4 v[56:59], v[120:121], off offset:1200
	s_nop 0
	v_lshl_add_u64 v[120:121], v[120:121], 0, s[10:11]
	global_load_dwordx4 v[60:63], v[120:121], off
	global_load_dwordx4 v[64:67], v[120:121], off offset:1200
	s_nop 0
	v_lshl_add_u64 v[120:121], v[120:121], 0, s[10:11]
	global_load_dwordx4 v[72:75], v[120:121], off
	global_load_dwordx4 v[76:79], v[120:121], off offset:1200
	s_nop 0
	v_lshl_add_u64 v[120:121], v[120:121], 0, s[10:11]
	global_load_dwordx4 v[80:83], v[120:121], off
	global_load_dwordx4 v[84:87], v[120:121], off offset:1200
	ds_read_b64 v[104:105], v122 offset:8
	ds_read_b64 v[106:107], v122 offset:520
	ds_read_b64 v[108:109], v122 offset:1032
	ds_read_b64 v[110:111], v122 offset:1544
	v_lshl_add_u64 v[120:121], v[120:121], 0, s[10:11]
	s_waitcnt vmcnt(10) lgkmcnt(4)
	v_pk_fma_f32 v[4:5], v[88:89], v[36:37], v[4:5] op_sel_hi:[0,1,1]
	v_pk_fma_f32 v[6:7], v[88:89], v[38:39], v[6:7] op_sel_hi:[0,1,1]
	v_pk_fma_f32 v[8:9], v[90:91], v[36:37], v[8:9] op_sel_hi:[0,1,1]
	v_pk_fma_f32 v[10:11], v[90:91], v[38:39], v[10:11] op_sel_hi:[0,1,1]
	v_pk_fma_f32 v[12:13], v[92:93], v[36:37], v[12:13] op_sel_hi:[0,1,1]
	v_pk_fma_f32 v[14:15], v[92:93], v[38:39], v[14:15] op_sel_hi:[0,1,1]
	v_pk_fma_f32 v[16:17], v[94:95], v[36:37], v[16:17] op_sel_hi:[0,1,1]
	v_pk_fma_f32 v[18:19], v[94:95], v[38:39], v[18:19] op_sel_hi:[0,1,1]
	v_pk_fma_f32 v[4:5], v[88:89], v[40:41], v[4:5] op_sel:[1,0,0]
	v_pk_fma_f32 v[6:7], v[88:89], v[42:43], v[6:7] op_sel:[1,0,0]
	v_pk_fma_f32 v[8:9], v[90:91], v[40:41], v[8:9] op_sel:[1,0,0]
	v_pk_fma_f32 v[10:11], v[90:91], v[42:43], v[10:11] op_sel:[1,0,0]
	v_pk_fma_f32 v[12:13], v[92:93], v[40:41], v[12:13] op_sel:[1,0,0]
	v_pk_fma_f32 v[14:15], v[92:93], v[42:43], v[14:15] op_sel:[1,0,0]
	v_pk_fma_f32 v[16:17], v[94:95], v[40:41], v[16:17] op_sel:[1,0,0]
	v_pk_fma_f32 v[18:19], v[94:95], v[42:43], v[18:19] op_sel:[1,0,0]
	global_load_dwordx4 v[36:39], v[120:121], off
	global_load_dwordx4 v[40:43], v[120:121], off offset:1200
	ds_read_b64 v[88:89], v122 offset:16
	ds_read_b64 v[90:91], v122 offset:528
	ds_read_b64 v[92:93], v122 offset:1040
	ds_read_b64 v[94:95], v122 offset:1552
	v_lshl_add_u64 v[120:121], v[120:121], 0, s[10:11]
	s_waitcnt vmcnt(10) lgkmcnt(4)
	v_pk_fma_f32 v[4:5], v[104:105], v[44:45], v[4:5] op_sel_hi:[0,1,1]
	v_pk_fma_f32 v[6:7], v[104:105], v[46:47], v[6:7] op_sel_hi:[0,1,1]
	v_pk_fma_f32 v[8:9], v[106:107], v[44:45], v[8:9] op_sel_hi:[0,1,1]
	v_pk_fma_f32 v[10:11], v[106:107], v[46:47], v[10:11] op_sel_hi:[0,1,1]
	v_pk_fma_f32 v[12:13], v[108:109], v[44:45], v[12:13] op_sel_hi:[0,1,1]
	v_pk_fma_f32 v[14:15], v[108:109], v[46:47], v[14:15] op_sel_hi:[0,1,1]
	v_pk_fma_f32 v[16:17], v[110:111], v[44:45], v[16:17] op_sel_hi:[0,1,1]
	v_pk_fma_f32 v[18:19], v[110:111], v[46:47], v[18:19] op_sel_hi:[0,1,1]
	v_pk_fma_f32 v[4:5], v[104:105], v[48:49], v[4:5] op_sel:[1,0,0]
	v_pk_fma_f32 v[6:7], v[104:105], v[50:51], v[6:7] op_sel:[1,0,0]
	v_pk_fma_f32 v[8:9], v[106:107], v[48:49], v[8:9] op_sel:[1,0,0]
	v_pk_fma_f32 v[10:11], v[106:107], v[50:51], v[10:11] op_sel:[1,0,0]
	v_pk_fma_f32 v[12:13], v[108:109], v[48:49], v[12:13] op_sel:[1,0,0]
	v_pk_fma_f32 v[14:15], v[108:109], v[50:51], v[14:15] op_sel:[1,0,0]
	v_pk_fma_f32 v[16:17], v[110:111], v[48:49], v[16:17] op_sel:[1,0,0]
	v_pk_fma_f32 v[18:19], v[110:111], v[50:51], v[18:19] op_sel:[1,0,0]
	global_load_dwordx4 v[44:47], v[120:121], off
	global_load_dwordx4 v[48:51], v[120:121], off offset:1200
	ds_read_b64 v[104:105], v122 offset:24
	ds_read_b64 v[106:107], v122 offset:536
	ds_read_b64 v[108:109], v122 offset:1048
	ds_read_b64 v[110:111], v122 offset:1560
	v_lshl_add_u64 v[120:121], v[120:121], 0, s[10:11]
	s_waitcnt vmcnt(10) lgkmcnt(4)
	v_pk_fma_f32 v[4:5], v[88:89], v[52:53], v[4:5] op_sel_hi:[0,1,1]
	v_pk_fma_f32 v[6:7], v[88:89], v[54:55], v[6:7] op_sel_hi:[0,1,1]
	v_pk_fma_f32 v[8:9], v[90:91], v[52:53], v[8:9] op_sel_hi:[0,1,1]
	v_pk_fma_f32 v[10:11], v[90:91], v[54:55], v[10:11] op_sel_hi:[0,1,1]
	v_pk_fma_f32 v[12:13], v[92:93], v[52:53], v[12:13] op_sel_hi:[0,1,1]
	v_pk_fma_f32 v[14:15], v[92:93], v[54:55], v[14:15] op_sel_hi:[0,1,1]
	v_pk_fma_f32 v[16:17], v[94:95], v[52:53], v[16:17] op_sel_hi:[0,1,1]
	v_pk_fma_f32 v[18:19], v[94:95], v[54:55], v[18:19] op_sel_hi:[0,1,1]
	v_pk_fma_f32 v[4:5], v[88:89], v[56:57], v[4:5] op_sel:[1,0,0]
	v_pk_fma_f32 v[6:7], v[88:89], v[58:59], v[6:7] op_sel:[1,0,0]
	v_pk_fma_f32 v[8:9], v[90:91], v[56:57], v[8:9] op_sel:[1,0,0]
	v_pk_fma_f32 v[10:11], v[90:91], v[58:59], v[10:11] op_sel:[1,0,0]
	v_pk_fma_f32 v[12:13], v[92:93], v[56:57], v[12:13] op_sel:[1,0,0]
	v_pk_fma_f32 v[14:15], v[92:93], v[58:59], v[14:15] op_sel:[1,0,0]
	v_pk_fma_f32 v[16:17], v[94:95], v[56:57], v[16:17] op_sel:[1,0,0]
	v_pk_fma_f32 v[18:19], v[94:95], v[58:59], v[18:19] op_sel:[1,0,0]
	global_load_dwordx4 v[52:55], v[120:121], off
	global_load_dwordx4 v[56:59], v[120:121], off offset:1200
	ds_read_b64 v[88:89], v122 offset:32
	ds_read_b64 v[90:91], v122 offset:544
	ds_read_b64 v[92:93], v122 offset:1056
	ds_read_b64 v[94:95], v122 offset:1568
	v_lshl_add_u64 v[120:121], v[120:121], 0, s[10:11]
	s_waitcnt vmcnt(10) lgkmcnt(4)
	v_pk_fma_f32 v[4:5], v[104:105], v[60:61], v[4:5] op_sel_hi:[0,1,1]
	v_pk_fma_f32 v[6:7], v[104:105], v[62:63], v[6:7] op_sel_hi:[0,1,1]
	v_pk_fma_f32 v[8:9], v[106:107], v[60:61], v[8:9] op_sel_hi:[0,1,1]
	v_pk_fma_f32 v[10:11], v[106:107], v[62:63], v[10:11] op_sel_hi:[0,1,1]
	v_pk_fma_f32 v[12:13], v[108:109], v[60:61], v[12:13] op_sel_hi:[0,1,1]
	v_pk_fma_f32 v[14:15], v[108:109], v[62:63], v[14:15] op_sel_hi:[0,1,1]
	v_pk_fma_f32 v[16:17], v[110:111], v[60:61], v[16:17] op_sel_hi:[0,1,1]
	v_pk_fma_f32 v[18:19], v[110:111], v[62:63], v[18:19] op_sel_hi:[0,1,1]
	v_pk_fma_f32 v[4:5], v[104:105], v[64:65], v[4:5] op_sel:[1,0,0]
	v_pk_fma_f32 v[6:7], v[104:105], v[66:67], v[6:7] op_sel:[1,0,0]
	v_pk_fma_f32 v[8:9], v[106:107], v[64:65], v[8:9] op_sel:[1,0,0]
	v_pk_fma_f32 v[10:11], v[106:107], v[66:67], v[10:11] op_sel:[1,0,0]
	v_pk_fma_f32 v[12:13], v[108:109], v[64:65], v[12:13] op_sel:[1,0,0]
	v_pk_fma_f32 v[14:15], v[108:109], v[66:67], v[14:15] op_sel:[1,0,0]
	v_pk_fma_f32 v[16:17], v[110:111], v[64:65], v[16:17] op_sel:[1,0,0]
	v_pk_fma_f32 v[18:19], v[110:111], v[66:67], v[18:19] op_sel:[1,0,0]
	global_load_dwordx4 v[60:63], v[120:121], off
	global_load_dwordx4 v[64:67], v[120:121], off offset:1200
	ds_read_b64 v[104:105], v122 offset:40
	ds_read_b64 v[106:107], v122 offset:552
	ds_read_b64 v[108:109], v122 offset:1064
	ds_read_b64 v[110:111], v122 offset:1576
	v_lshl_add_u64 v[120:121], v[120:121], 0, s[10:11]
	s_waitcnt vmcnt(10) lgkmcnt(4)
	v_pk_fma_f32 v[4:5], v[88:89], v[72:73], v[4:5] op_sel_hi:[0,1,1]
	v_pk_fma_f32 v[6:7], v[88:89], v[74:75], v[6:7] op_sel_hi:[0,1,1]
	v_pk_fma_f32 v[8:9], v[90:91], v[72:73], v[8:9] op_sel_hi:[0,1,1]
	v_pk_fma_f32 v[10:11], v[90:91], v[74:75], v[10:11] op_sel_hi:[0,1,1]
	v_pk_fma_f32 v[12:13], v[92:93], v[72:73], v[12:13] op_sel_hi:[0,1,1]
	v_pk_fma_f32 v[14:15], v[92:93], v[74:75], v[14:15] op_sel_hi:[0,1,1]
	v_pk_fma_f32 v[16:17], v[94:95], v[72:73], v[16:17] op_sel_hi:[0,1,1]
	v_pk_fma_f32 v[18:19], v[94:95], v[74:75], v[18:19] op_sel_hi:[0,1,1]
	v_pk_fma_f32 v[4:5], v[88:89], v[76:77], v[4:5] op_sel:[1,0,0]
	v_pk_fma_f32 v[6:7], v[88:89], v[78:79], v[6:7] op_sel:[1,0,0]
	v_pk_fma_f32 v[8:9], v[90:91], v[76:77], v[8:9] op_sel:[1,0,0]
	v_pk_fma_f32 v[10:11], v[90:91], v[78:79], v[10:11] op_sel:[1,0,0]
	v_pk_fma_f32 v[12:13], v[92:93], v[76:77], v[12:13] op_sel:[1,0,0]
	v_pk_fma_f32 v[14:15], v[92:93], v[78:79], v[14:15] op_sel:[1,0,0]
	v_pk_fma_f32 v[16:17], v[94:95], v[76:77], v[16:17] op_sel:[1,0,0]
	v_pk_fma_f32 v[18:19], v[94:95], v[78:79], v[18:19] op_sel:[1,0,0]
	global_load_dwordx4 v[72:75], v[120:121], off
	global_load_dwordx4 v[76:79], v[120:121], off offset:1200
	ds_read_b64 v[88:89], v122 offset:48
	ds_read_b64 v[90:91], v122 offset:560
	ds_read_b64 v[92:93], v122 offset:1072
	ds_read_b64 v[94:95], v122 offset:1584
	v_lshl_add_u64 v[120:121], v[120:121], 0, s[10:11]
	s_waitcnt vmcnt(10) lgkmcnt(4)
	v_pk_fma_f32 v[4:5], v[104:105], v[80:81], v[4:5] op_sel_hi:[0,1,1]
	v_pk_fma_f32 v[6:7], v[104:105], v[82:83], v[6:7] op_sel_hi:[0,1,1]
	v_pk_fma_f32 v[8:9], v[106:107], v[80:81], v[8:9] op_sel_hi:[0,1,1]
	v_pk_fma_f32 v[10:11], v[106:107], v[82:83], v[10:11] op_sel_hi:[0,1,1]
	v_pk_fma_f32 v[12:13], v[108:109], v[80:81], v[12:13] op_sel_hi:[0,1,1]
	v_pk_fma_f32 v[14:15], v[108:109], v[82:83], v[14:15] op_sel_hi:[0,1,1]
	v_pk_fma_f32 v[16:17], v[110:111], v[80:81], v[16:17] op_sel_hi:[0,1,1]
	v_pk_fma_f32 v[18:19], v[110:111], v[82:83], v[18:19] op_sel_hi:[0,1,1]
	v_pk_fma_f32 v[4:5], v[104:105], v[84:85], v[4:5] op_sel:[1,0,0]
	v_pk_fma_f32 v[6:7], v[104:105], v[86:87], v[6:7] op_sel:[1,0,0]
	v_pk_fma_f32 v[8:9], v[106:107], v[84:85], v[8:9] op_sel:[1,0,0]
	v_pk_fma_f32 v[10:11], v[106:107], v[86:87], v[10:11] op_sel:[1,0,0]
	v_pk_fma_f32 v[12:13], v[108:109], v[84:85], v[12:13] op_sel:[1,0,0]
	v_pk_fma_f32 v[14:15], v[108:109], v[86:87], v[14:15] op_sel:[1,0,0]
	v_pk_fma_f32 v[16:17], v[110:111], v[84:85], v[16:17] op_sel:[1,0,0]
	v_pk_fma_f32 v[18:19], v[110:111], v[86:87], v[18:19] op_sel:[1,0,0]
	global_load_dwordx4 v[80:83], v[120:121], off
	global_load_dwordx4 v[84:87], v[120:121], off offset:1200
	ds_read_b64 v[104:105], v122 offset:56
	ds_read_b64 v[106:107], v122 offset:568
	ds_read_b64 v[108:109], v122 offset:1080
	ds_read_b64 v[110:111], v122 offset:1592
	v_lshl_add_u64 v[120:121], v[120:121], 0, s[10:11]
	s_waitcnt vmcnt(10) lgkmcnt(4)
	v_pk_fma_f32 v[4:5], v[88:89], v[36:37], v[4:5] op_sel_hi:[0,1,1]
	v_pk_fma_f32 v[6:7], v[88:89], v[38:39], v[6:7] op_sel_hi:[0,1,1]
	v_pk_fma_f32 v[8:9], v[90:91], v[36:37], v[8:9] op_sel_hi:[0,1,1]
	v_pk_fma_f32 v[10:11], v[90:91], v[38:39], v[10:11] op_sel_hi:[0,1,1]
	v_pk_fma_f32 v[12:13], v[92:93], v[36:37], v[12:13] op_sel_hi:[0,1,1]
	v_pk_fma_f32 v[14:15], v[92:93], v[38:39], v[14:15] op_sel_hi:[0,1,1]
	v_pk_fma_f32 v[16:17], v[94:95], v[36:37], v[16:17] op_sel_hi:[0,1,1]
	v_pk_fma_f32 v[18:19], v[94:95], v[38:39], v[18:19] op_sel_hi:[0,1,1]
	v_pk_fma_f32 v[4:5], v[88:89], v[40:41], v[4:5] op_sel:[1,0,0]
	v_pk_fma_f32 v[6:7], v[88:89], v[42:43], v[6:7] op_sel:[1,0,0]
	v_pk_fma_f32 v[8:9], v[90:91], v[40:41], v[8:9] op_sel:[1,0,0]
	v_pk_fma_f32 v[10:11], v[90:91], v[42:43], v[10:11] op_sel:[1,0,0]
	v_pk_fma_f32 v[12:13], v[92:93], v[40:41], v[12:13] op_sel:[1,0,0]
	v_pk_fma_f32 v[14:15], v[92:93], v[42:43], v[14:15] op_sel:[1,0,0]
	v_pk_fma_f32 v[16:17], v[94:95], v[40:41], v[16:17] op_sel:[1,0,0]
	v_pk_fma_f32 v[18:19], v[94:95], v[42:43], v[18:19] op_sel:[1,0,0]
	global_load_dwordx4 v[36:39], v[120:121], off
	global_load_dwordx4 v[40:43], v[120:121], off offset:1200
	ds_read_b64 v[88:89], v122 offset:64
	ds_read_b64 v[90:91], v122 offset:576
	ds_read_b64 v[92:93], v122 offset:1088
	ds_read_b64 v[94:95], v122 offset:1600
	v_lshl_add_u64 v[120:121], v[120:121], 0, s[10:11]
	s_waitcnt vmcnt(10) lgkmcnt(4)
	v_pk_fma_f32 v[4:5], v[104:105], v[44:45], v[4:5] op_sel_hi:[0,1,1]
	v_pk_fma_f32 v[6:7], v[104:105], v[46:47], v[6:7] op_sel_hi:[0,1,1]
	v_pk_fma_f32 v[8:9], v[106:107], v[44:45], v[8:9] op_sel_hi:[0,1,1]
	v_pk_fma_f32 v[10:11], v[106:107], v[46:47], v[10:11] op_sel_hi:[0,1,1]
	v_pk_fma_f32 v[12:13], v[108:109], v[44:45], v[12:13] op_sel_hi:[0,1,1]
	v_pk_fma_f32 v[14:15], v[108:109], v[46:47], v[14:15] op_sel_hi:[0,1,1]
	v_pk_fma_f32 v[16:17], v[110:111], v[44:45], v[16:17] op_sel_hi:[0,1,1]
	v_pk_fma_f32 v[18:19], v[110:111], v[46:47], v[18:19] op_sel_hi:[0,1,1]
	v_pk_fma_f32 v[4:5], v[104:105], v[48:49], v[4:5] op_sel:[1,0,0]
	v_pk_fma_f32 v[6:7], v[104:105], v[50:51], v[6:7] op_sel:[1,0,0]
	v_pk_fma_f32 v[8:9], v[106:107], v[48:49], v[8:9] op_sel:[1,0,0]
	v_pk_fma_f32 v[10:11], v[106:107], v[50:51], v[10:11] op_sel:[1,0,0]
	v_pk_fma_f32 v[12:13], v[108:109], v[48:49], v[12:13] op_sel:[1,0,0]
	v_pk_fma_f32 v[14:15], v[108:109], v[50:51], v[14:15] op_sel:[1,0,0]
	v_pk_fma_f32 v[16:17], v[110:111], v[48:49], v[16:17] op_sel:[1,0,0]
	v_pk_fma_f32 v[18:19], v[110:111], v[50:51], v[18:19] op_sel:[1,0,0]
	global_load_dwordx4 v[44:47], v[120:121], off
	global_load_dwordx4 v[48:51], v[120:121], off offset:1200
	ds_read_b64 v[104:105], v122 offset:72
	ds_read_b64 v[106:107], v122 offset:584
	ds_read_b64 v[108:109], v122 offset:1096
	ds_read_b64 v[110:111], v122 offset:1608
	v_lshl_add_u64 v[120:121], v[120:121], 0, s[10:11]
	s_waitcnt vmcnt(10) lgkmcnt(4)
	v_pk_fma_f32 v[4:5], v[88:89], v[52:53], v[4:5] op_sel_hi:[0,1,1]
	v_pk_fma_f32 v[6:7], v[88:89], v[54:55], v[6:7] op_sel_hi:[0,1,1]
	v_pk_fma_f32 v[8:9], v[90:91], v[52:53], v[8:9] op_sel_hi:[0,1,1]
	v_pk_fma_f32 v[10:11], v[90:91], v[54:55], v[10:11] op_sel_hi:[0,1,1]
	v_pk_fma_f32 v[12:13], v[92:93], v[52:53], v[12:13] op_sel_hi:[0,1,1]
	v_pk_fma_f32 v[14:15], v[92:93], v[54:55], v[14:15] op_sel_hi:[0,1,1]
	v_pk_fma_f32 v[16:17], v[94:95], v[52:53], v[16:17] op_sel_hi:[0,1,1]
	v_pk_fma_f32 v[18:19], v[94:95], v[54:55], v[18:19] op_sel_hi:[0,1,1]
	v_pk_fma_f32 v[4:5], v[88:89], v[56:57], v[4:5] op_sel:[1,0,0]
	v_pk_fma_f32 v[6:7], v[88:89], v[58:59], v[6:7] op_sel:[1,0,0]
	v_pk_fma_f32 v[8:9], v[90:91], v[56:57], v[8:9] op_sel:[1,0,0]
	v_pk_fma_f32 v[10:11], v[90:91], v[58:59], v[10:11] op_sel:[1,0,0]
	v_pk_fma_f32 v[12:13], v[92:93], v[56:57], v[12:13] op_sel:[1,0,0]
	v_pk_fma_f32 v[14:15], v[92:93], v[58:59], v[14:15] op_sel:[1,0,0]
	v_pk_fma_f32 v[16:17], v[94:95], v[56:57], v[16:17] op_sel:[1,0,0]
	v_pk_fma_f32 v[18:19], v[94:95], v[58:59], v[18:19] op_sel:[1,0,0]
	global_load_dwordx4 v[52:55], v[120:121], off
	global_load_dwordx4 v[56:59], v[120:121], off offset:1200
	ds_read_b64 v[88:89], v122 offset:80
	ds_read_b64 v[90:91], v122 offset:592
	ds_read_b64 v[92:93], v122 offset:1104
	ds_read_b64 v[94:95], v122 offset:1616
	v_lshl_add_u64 v[120:121], v[120:121], 0, s[10:11]
	s_waitcnt vmcnt(10) lgkmcnt(4)
	v_pk_fma_f32 v[4:5], v[104:105], v[60:61], v[4:5] op_sel_hi:[0,1,1]
	v_pk_fma_f32 v[6:7], v[104:105], v[62:63], v[6:7] op_sel_hi:[0,1,1]
	v_pk_fma_f32 v[8:9], v[106:107], v[60:61], v[8:9] op_sel_hi:[0,1,1]
	v_pk_fma_f32 v[10:11], v[106:107], v[62:63], v[10:11] op_sel_hi:[0,1,1]
	v_pk_fma_f32 v[12:13], v[108:109], v[60:61], v[12:13] op_sel_hi:[0,1,1]
	v_pk_fma_f32 v[14:15], v[108:109], v[62:63], v[14:15] op_sel_hi:[0,1,1]
	v_pk_fma_f32 v[16:17], v[110:111], v[60:61], v[16:17] op_sel_hi:[0,1,1]
	v_pk_fma_f32 v[18:19], v[110:111], v[62:63], v[18:19] op_sel_hi:[0,1,1]
	v_pk_fma_f32 v[4:5], v[104:105], v[64:65], v[4:5] op_sel:[1,0,0]
	v_pk_fma_f32 v[6:7], v[104:105], v[66:67], v[6:7] op_sel:[1,0,0]
	v_pk_fma_f32 v[8:9], v[106:107], v[64:65], v[8:9] op_sel:[1,0,0]
	v_pk_fma_f32 v[10:11], v[106:107], v[66:67], v[10:11] op_sel:[1,0,0]
	v_pk_fma_f32 v[12:13], v[108:109], v[64:65], v[12:13] op_sel:[1,0,0]
	v_pk_fma_f32 v[14:15], v[108:109], v[66:67], v[14:15] op_sel:[1,0,0]
	v_pk_fma_f32 v[16:17], v[110:111], v[64:65], v[16:17] op_sel:[1,0,0]
	v_pk_fma_f32 v[18:19], v[110:111], v[66:67], v[18:19] op_sel:[1,0,0]
	global_load_dwordx4 v[60:63], v[120:121], off
	global_load_dwordx4 v[64:67], v[120:121], off offset:1200
	ds_read_b64 v[104:105], v122 offset:88
	ds_read_b64 v[106:107], v122 offset:600
	ds_read_b64 v[108:109], v122 offset:1112
	ds_read_b64 v[110:111], v122 offset:1624
	v_lshl_add_u64 v[120:121], v[120:121], 0, s[10:11]
	s_waitcnt vmcnt(10) lgkmcnt(4)
	v_pk_fma_f32 v[4:5], v[88:89], v[72:73], v[4:5] op_sel_hi:[0,1,1]
	v_pk_fma_f32 v[6:7], v[88:89], v[74:75], v[6:7] op_sel_hi:[0,1,1]
	v_pk_fma_f32 v[8:9], v[90:91], v[72:73], v[8:9] op_sel_hi:[0,1,1]
	v_pk_fma_f32 v[10:11], v[90:91], v[74:75], v[10:11] op_sel_hi:[0,1,1]
	v_pk_fma_f32 v[12:13], v[92:93], v[72:73], v[12:13] op_sel_hi:[0,1,1]
	v_pk_fma_f32 v[14:15], v[92:93], v[74:75], v[14:15] op_sel_hi:[0,1,1]
	v_pk_fma_f32 v[16:17], v[94:95], v[72:73], v[16:17] op_sel_hi:[0,1,1]
	v_pk_fma_f32 v[18:19], v[94:95], v[74:75], v[18:19] op_sel_hi:[0,1,1]
	v_pk_fma_f32 v[4:5], v[88:89], v[76:77], v[4:5] op_sel:[1,0,0]
	v_pk_fma_f32 v[6:7], v[88:89], v[78:79], v[6:7] op_sel:[1,0,0]
	v_pk_fma_f32 v[8:9], v[90:91], v[76:77], v[8:9] op_sel:[1,0,0]
	v_pk_fma_f32 v[10:11], v[90:91], v[78:79], v[10:11] op_sel:[1,0,0]
	v_pk_fma_f32 v[12:13], v[92:93], v[76:77], v[12:13] op_sel:[1,0,0]
	v_pk_fma_f32 v[14:15], v[92:93], v[78:79], v[14:15] op_sel:[1,0,0]
	v_pk_fma_f32 v[16:17], v[94:95], v[76:77], v[16:17] op_sel:[1,0,0]
	v_pk_fma_f32 v[18:19], v[94:95], v[78:79], v[18:19] op_sel:[1,0,0]
	ds_read_b64 v[88:89], v122 offset:96
	ds_read_b64 v[90:91], v122 offset:608
	ds_read_b64 v[92:93], v122 offset:1120
	ds_read_b64 v[94:95], v122 offset:1632
	s_waitcnt vmcnt(8) lgkmcnt(4)
	v_pk_fma_f32 v[4:5], v[104:105], v[80:81], v[4:5] op_sel_hi:[0,1,1]
	v_pk_fma_f32 v[6:7], v[104:105], v[82:83], v[6:7] op_sel_hi:[0,1,1]
	v_pk_fma_f32 v[8:9], v[106:107], v[80:81], v[8:9] op_sel_hi:[0,1,1]
	v_pk_fma_f32 v[10:11], v[106:107], v[82:83], v[10:11] op_sel_hi:[0,1,1]
	v_pk_fma_f32 v[12:13], v[108:109], v[80:81], v[12:13] op_sel_hi:[0,1,1]
	v_pk_fma_f32 v[14:15], v[108:109], v[82:83], v[14:15] op_sel_hi:[0,1,1]
	v_pk_fma_f32 v[16:17], v[110:111], v[80:81], v[16:17] op_sel_hi:[0,1,1]
	v_pk_fma_f32 v[18:19], v[110:111], v[82:83], v[18:19] op_sel_hi:[0,1,1]
	v_pk_fma_f32 v[4:5], v[104:105], v[84:85], v[4:5] op_sel:[1,0,0]
	v_pk_fma_f32 v[6:7], v[104:105], v[86:87], v[6:7] op_sel:[1,0,0]
	v_pk_fma_f32 v[8:9], v[106:107], v[84:85], v[8:9] op_sel:[1,0,0]
	v_pk_fma_f32 v[10:11], v[106:107], v[86:87], v[10:11] op_sel:[1,0,0]
	v_pk_fma_f32 v[12:13], v[108:109], v[84:85], v[12:13] op_sel:[1,0,0]
	v_pk_fma_f32 v[14:15], v[108:109], v[86:87], v[14:15] op_sel:[1,0,0]
	v_pk_fma_f32 v[16:17], v[110:111], v[84:85], v[16:17] op_sel:[1,0,0]
	v_pk_fma_f32 v[18:19], v[110:111], v[86:87], v[18:19] op_sel:[1,0,0]
	ds_read_b64 v[104:105], v122 offset:104
	ds_read_b64 v[106:107], v122 offset:616
	ds_read_b64 v[108:109], v122 offset:1128
	ds_read_b64 v[110:111], v122 offset:1640
	s_waitcnt vmcnt(6) lgkmcnt(4)
	v_pk_fma_f32 v[4:5], v[88:89], v[36:37], v[4:5] op_sel_hi:[0,1,1]
	v_pk_fma_f32 v[6:7], v[88:89], v[38:39], v[6:7] op_sel_hi:[0,1,1]
	v_pk_fma_f32 v[8:9], v[90:91], v[36:37], v[8:9] op_sel_hi:[0,1,1]
	v_pk_fma_f32 v[10:11], v[90:91], v[38:39], v[10:11] op_sel_hi:[0,1,1]
	v_pk_fma_f32 v[12:13], v[92:93], v[36:37], v[12:13] op_sel_hi:[0,1,1]
	v_pk_fma_f32 v[14:15], v[92:93], v[38:39], v[14:15] op_sel_hi:[0,1,1]
	v_pk_fma_f32 v[16:17], v[94:95], v[36:37], v[16:17] op_sel_hi:[0,1,1]
	v_pk_fma_f32 v[18:19], v[94:95], v[38:39], v[18:19] op_sel_hi:[0,1,1]
	v_pk_fma_f32 v[4:5], v[88:89], v[40:41], v[4:5] op_sel:[1,0,0]
	v_pk_fma_f32 v[6:7], v[88:89], v[42:43], v[6:7] op_sel:[1,0,0]
	v_pk_fma_f32 v[8:9], v[90:91], v[40:41], v[8:9] op_sel:[1,0,0]
	v_pk_fma_f32 v[10:11], v[90:91], v[42:43], v[10:11] op_sel:[1,0,0]
	v_pk_fma_f32 v[12:13], v[92:93], v[40:41], v[12:13] op_sel:[1,0,0]
	v_pk_fma_f32 v[14:15], v[92:93], v[42:43], v[14:15] op_sel:[1,0,0]
	v_pk_fma_f32 v[16:17], v[94:95], v[40:41], v[16:17] op_sel:[1,0,0]
	v_pk_fma_f32 v[18:19], v[94:95], v[42:43], v[18:19] op_sel:[1,0,0]
	ds_read_b64 v[88:89], v122 offset:112
	ds_read_b64 v[90:91], v122 offset:624
	ds_read_b64 v[92:93], v122 offset:1136
	ds_read_b64 v[94:95], v122 offset:1648
	s_waitcnt vmcnt(4) lgkmcnt(4)
	v_pk_fma_f32 v[4:5], v[104:105], v[44:45], v[4:5] op_sel_hi:[0,1,1]
	v_pk_fma_f32 v[6:7], v[104:105], v[46:47], v[6:7] op_sel_hi:[0,1,1]
	v_pk_fma_f32 v[8:9], v[106:107], v[44:45], v[8:9] op_sel_hi:[0,1,1]
	v_pk_fma_f32 v[10:11], v[106:107], v[46:47], v[10:11] op_sel_hi:[0,1,1]
	v_pk_fma_f32 v[12:13], v[108:109], v[44:45], v[12:13] op_sel_hi:[0,1,1]
	v_pk_fma_f32 v[14:15], v[108:109], v[46:47], v[14:15] op_sel_hi:[0,1,1]
	v_pk_fma_f32 v[16:17], v[110:111], v[44:45], v[16:17] op_sel_hi:[0,1,1]
	v_pk_fma_f32 v[18:19], v[110:111], v[46:47], v[18:19] op_sel_hi:[0,1,1]
	v_pk_fma_f32 v[4:5], v[104:105], v[48:49], v[4:5] op_sel:[1,0,0]
	v_pk_fma_f32 v[6:7], v[104:105], v[50:51], v[6:7] op_sel:[1,0,0]
	v_pk_fma_f32 v[8:9], v[106:107], v[48:49], v[8:9] op_sel:[1,0,0]
	v_pk_fma_f32 v[10:11], v[106:107], v[50:51], v[10:11] op_sel:[1,0,0]
	v_pk_fma_f32 v[12:13], v[108:109], v[48:49], v[12:13] op_sel:[1,0,0]
	v_pk_fma_f32 v[14:15], v[108:109], v[50:51], v[14:15] op_sel:[1,0,0]
	v_pk_fma_f32 v[16:17], v[110:111], v[48:49], v[16:17] op_sel:[1,0,0]
	v_pk_fma_f32 v[18:19], v[110:111], v[50:51], v[18:19] op_sel:[1,0,0]
	ds_read_b64 v[104:105], v122 offset:120
	ds_read_b64 v[106:107], v122 offset:632
	ds_read_b64 v[108:109], v122 offset:1144
	ds_read_b64 v[110:111], v122 offset:1656
	s_waitcnt vmcnt(2) lgkmcnt(4)
	v_pk_fma_f32 v[4:5], v[88:89], v[52:53], v[4:5] op_sel_hi:[0,1,1]
	v_pk_fma_f32 v[6:7], v[88:89], v[54:55], v[6:7] op_sel_hi:[0,1,1]
	v_pk_fma_f32 v[8:9], v[90:91], v[52:53], v[8:9] op_sel_hi:[0,1,1]
	v_pk_fma_f32 v[10:11], v[90:91], v[54:55], v[10:11] op_sel_hi:[0,1,1]
	v_pk_fma_f32 v[12:13], v[92:93], v[52:53], v[12:13] op_sel_hi:[0,1,1]
	v_pk_fma_f32 v[14:15], v[92:93], v[54:55], v[14:15] op_sel_hi:[0,1,1]
	v_pk_fma_f32 v[16:17], v[94:95], v[52:53], v[16:17] op_sel_hi:[0,1,1]
	v_pk_fma_f32 v[18:19], v[94:95], v[54:55], v[18:19] op_sel_hi:[0,1,1]
	v_pk_fma_f32 v[4:5], v[88:89], v[56:57], v[4:5] op_sel:[1,0,0]
	v_pk_fma_f32 v[6:7], v[88:89], v[58:59], v[6:7] op_sel:[1,0,0]
	v_pk_fma_f32 v[8:9], v[90:91], v[56:57], v[8:9] op_sel:[1,0,0]
	v_pk_fma_f32 v[10:11], v[90:91], v[58:59], v[10:11] op_sel:[1,0,0]
	v_pk_fma_f32 v[12:13], v[92:93], v[56:57], v[12:13] op_sel:[1,0,0]
	v_pk_fma_f32 v[14:15], v[92:93], v[58:59], v[14:15] op_sel:[1,0,0]
	v_pk_fma_f32 v[16:17], v[94:95], v[56:57], v[16:17] op_sel:[1,0,0]
	v_pk_fma_f32 v[18:19], v[94:95], v[58:59], v[18:19] op_sel:[1,0,0]
	s_waitcnt vmcnt(0) lgkmcnt(0)
	v_pk_fma_f32 v[4:5], v[104:105], v[60:61], v[4:5] op_sel_hi:[0,1,1]
	v_pk_fma_f32 v[6:7], v[104:105], v[62:63], v[6:7] op_sel_hi:[0,1,1]
	v_pk_fma_f32 v[8:9], v[106:107], v[60:61], v[8:9] op_sel_hi:[0,1,1]
	v_pk_fma_f32 v[10:11], v[106:107], v[62:63], v[10:11] op_sel_hi:[0,1,1]
	v_pk_fma_f32 v[12:13], v[108:109], v[60:61], v[12:13] op_sel_hi:[0,1,1]
	v_pk_fma_f32 v[14:15], v[108:109], v[62:63], v[14:15] op_sel_hi:[0,1,1]
	v_pk_fma_f32 v[16:17], v[110:111], v[60:61], v[16:17] op_sel_hi:[0,1,1]
	v_pk_fma_f32 v[18:19], v[110:111], v[62:63], v[18:19] op_sel_hi:[0,1,1]
	v_pk_fma_f32 v[4:5], v[104:105], v[64:65], v[4:5] op_sel:[1,0,0]
	v_pk_fma_f32 v[6:7], v[104:105], v[66:67], v[6:7] op_sel:[1,0,0]
	v_pk_fma_f32 v[8:9], v[106:107], v[64:65], v[8:9] op_sel:[1,0,0]
	v_pk_fma_f32 v[10:11], v[106:107], v[66:67], v[10:11] op_sel:[1,0,0]
	v_pk_fma_f32 v[12:13], v[108:109], v[64:65], v[12:13] op_sel:[1,0,0]
	v_pk_fma_f32 v[14:15], v[108:109], v[66:67], v[14:15] op_sel:[1,0,0]
	v_pk_fma_f32 v[16:17], v[110:111], v[64:65], v[16:17] op_sel:[1,0,0]
	v_pk_fma_f32 v[18:19], v[110:111], v[66:67], v[18:19] op_sel:[1,0,0]
	v_lshlrev_b32_e32 v2, 3, v123
	v_add_u32_e32 v2, 0x258, v2
	v_mov_b32_e32 v3, 0
	v_lshl_add_u64 v[100:101], s[12:13], 0, v[2:3]
	v_cmp_ne_u32_e32 vcc, 0, v124
	s_and_saveexec_b64 s[8:9], vcc
	v_add_u32_e32 v1, -1, v124
	v_mul_u32_u24_e32 v1, 0x5dc0, v1
	v_mov_b32_e32 v2, 0x112c0
	v_cmp_eq_u32_e32 vcc, 3, v124
	s_nop 1
	v_cndmask_b32_e32 v1, v1, v2, vcc
	v_add_u32_e32 v127, v126, v1
	ds_write_b128 v127, v[4:7]
	ds_write_b128 v127, v[8:11] offset:1200
	ds_write_b128 v127, v[12:15] offset:2400
	ds_write_b128 v127, v[16:19] offset:3600
.Latt3_join:
	s_mov_b64 exec, -1
	s_waitcnt lgkmcnt(0)
	s_barrier
	s_cmp_lt_u32 s4, 3
	s_cbranch_scc1 .Latt3_fin_hp
	s_cmp_eq_u32 s4, 10
	s_cbranch_scc1 .Latt3_fin_hh
	s_cmp_eq_u32 s4, 11
	s_cbranch_scc1 .Latt3_fin_hh
	s_cmp_eq_u32 s4, 6
	s_cbranch_scc1 .Latt3_pass
	s_cmp_eq_u32 s4, 7
	s_cbranch_scc1 .Latt3_pass
	s_endpgm
.Latt3_fin_hp:
	v_cmp_eq_u32_e32 vcc, 0, v124
	s_and_saveexec_b64 s[6:7], vcc
	s_cbranch_execz .Latt3_end
	s_movk_i32 s5, 0xe10
	v_add_u32_e32 v127, 0x112c0, v126
	v_mad_u64_u32 v[110:111], s[8:9], v70, s5, v[100:101]
	v_add_u32_e32 v1, 1, v70
	v_mad_u64_u32 v[112:113], s[8:9], v1, s5, v[100:101]
	v_add_u32_e32 v1, 2, v70
	v_mad_u64_u32 v[114:115], s[8:9], v1, s5, v[100:101]
	v_add_u32_e32 v1, 3, v70
	v_mad_u64_u32 v[116:117], s[8:9], v1, s5, v[100:101]
	ds_read_b128 v[36:39], v126
	ds_read_b128 v[40:43], v126 offset:24000
	ds_read_b128 v[44:47], v127
	s_waitcnt lgkmcnt(2)
	v_pk_add_f32 v[4:5], v[4:5], v[36:37]
	v_pk_add_f32 v[6:7], v[6:7], v[38:39]
	s_waitcnt lgkmcnt(1)
	v_pk_add_f32 v[4:5], v[4:5], v[40:41]
	v_pk_add_f32 v[6:7], v[6:7], v[42:43]
	s_waitcnt lgkmcnt(0)
	v_pk_add_f32 v[4:5], v[4:5], v[44:45]
	v_pk_add_f32 v[6:7], v[6:7], v[46:47]
	s_nop 0
	v_cvt_pk_f16_f32 v48, v4, v5
	v_cvt_pk_f16_f32 v49, v6, v7
	global_store_dwordx2 v[110:111], v[48:49], off
	ds_read_b128 v[36:39], v126 offset:1200
	ds_read_b128 v[40:43], v126 offset:25200
	ds_read_b128 v[44:47], v127 offset:1200
	s_waitcnt lgkmcnt(2)
	v_pk_add_f32 v[8:9], v[8:9], v[36:37]
	v_pk_add_f32 v[10:11], v[10:11], v[38:39]
	s_waitcnt lgkmcnt(1)
	v_pk_add_f32 v[8:9], v[8:9], v[40:41]
	v_pk_add_f32 v[10:11], v[10:11], v[42:43]
	s_waitcnt lgkmcnt(0)
	v_pk_add_f32 v[8:9], v[8:9], v[44:45]
	v_pk_add_f32 v[10:11], v[10:11], v[46:47]
	s_nop 0
	v_cvt_pk_f16_f32 v48, v8, v9
	v_cvt_pk_f16_f32 v49, v10, v11
	global_store_dwordx2 v[112:113], v[48:49], off
	ds_read_b128 v[36:39], v126 offset:2400
	ds_read_b128 v[40:43], v126 offset:26400
	ds_read_b128 v[44:47], v127 offset:2400
	s_waitcnt lgkmcnt(2)
	v_pk_add_f32 v[12:13], v[12:13], v[36:37]
	v_pk_add_f32 v[14:15], v[14:15], v[38:39]
	s_waitcnt lgkmcnt(1)
	v_pk_add_f32 v[12:13], v[12:13], v[40:41]
	v_pk_add_f32 v[14:15], v[14:15], v[42:43]
	s_waitcnt lgkmcnt(0)
	v_pk_add_f32 v[12:13], v[12:13], v[44:45]
	v_pk_add_f32 v[14:15], v[14:15], v[46:47]
	s_nop 0
	v_cvt_pk_f16_f32 v48, v12, v13
	v_cvt_pk_f16_f32 v49, v14, v15
	global_store_dwordx2 v[114:115], v[48:49], off
	ds_read_b128 v[36:39], v126 offset:3600
	ds_read_b128 v[40:43], v126 offset:27600
	ds_read_b128 v[44:47], v127 offset:3600
	s_waitcnt lgkmcnt(2)
	v_pk_add_f32 v[16:17], v[16:17], v[36:37]
	v_pk_add_f32 v[18:19], v[18:19], v[38:39]
	s_waitcnt lgkmcnt(1)
	v_pk_add_f32 v[16:17], v[16:17], v[40:41]
	v_pk_add_f32 v[18:19], v[18:19], v[42:43]
	s_waitcnt lgkmcnt(0)
	v_pk_add_f32 v[16:17], v[16:17], v[44:45]
	v_pk_add_f32 v[18:19], v[18:19], v[46:47]
	s_nop 0
	v_cvt_pk_f16_f32 v48, v16, v17
	v_cvt_pk_f16_f32 v49, v18, v19
	global_store_dwordx2 v[116:117], v[48:49], off
	ds_read_b128 v[36:39], v126 offset:4800
	ds_read_b128 v[40:43], v126 offset:28800
	ds_read_b128 v[44:47], v127 offset:4800
	s_waitcnt lgkmcnt(2)
	v_pk_add_f32 v[20:21], v[20:21], v[36:37]
	v_pk_add_f32 v[22:23], v[22:23], v[38:39]
	s_waitcnt lgkmcnt(1)
	v_pk_add_f32 v[20:21], v[20:21], v[40:41]
	v_pk_add_f32 v[22:23], v[22:23], v[42:43]
	s_waitcnt lgkmcnt(0)
	v_pk_add_f32 v[20:21], v[20:21], v[44:45]
	v_pk_add_f32 v[22:23], v[22:23], v[46:47]
	s_nop 0
	v_cvt_pk_f16_f32 v48, v20, v21
	v_cvt_pk_f16_f32 v49, v22, v23
	global_store_dwordx2 v[110:111], v[48:49], off offset:600
	ds_read_b128 v[36:39], v126 offset:6000
	ds_read_b128 v[40:43], v126 offset:30000
	ds_read_b128 v[44:47], v127 offset:6000
	s_waitcnt lgkmcnt(2)
	v_pk_add_f32 v[24:25], v[24:25], v[36:37]
	v_pk_add_f32 v[26:27], v[26:27], v[38:39]
	s_waitcnt lgkmcnt(1)
	v_pk_add_f32 v[24:25], v[24:25], v[40:41]
	v_pk_add_f32 v[26:27], v[26:27], v[42:43]
	s_waitcnt lgkmcnt(0)
	v_pk_add_f32 v[24:25], v[24:25], v[44:45]
	v_pk_add_f32 v[26:27], v[26:27], v[46:47]
	s_nop 0
	v_cvt_pk_f16_f32 v48, v24, v25
	v_cvt_pk_f16_f32 v49, v26, v27
	global_store_dwordx2 v[112:113], v[48:49], off offset:600
	ds_read_b128 v[36:39], v126 offset:7200
	ds_read_b128 v[40:43], v126 offset:31200
	ds_read_b128 v[44:47], v127 offset:7200
	s_waitcnt lgkmcnt(2)
	v_pk_add_f32 v[28:29], v[28:29], v[36:37]
	v_pk_add_f32 v[30:31], v[30:31], v[38:39]
	s_waitcnt lgkmcnt(1)
	v_pk_add_f32 v[28:29], v[28:29], v[40:41]
	v_pk_add_f32 v[30:31], v[30:31], v[42:43]
	s_waitcnt lgkmcnt(0)
	v_pk_add_f32 v[28:29], v[28:29], v[44:45]
	v_pk_add_f32 v[30:31], v[30:31], v[46:47]
	s_nop 0
	v_cvt_pk_f16_f32 v48, v28, v29
	v_cvt_pk_f16_f32 v49, v30, v31
	global_store_dwordx2 v[114:115], v[48:49], off offset:600
	ds_read_b128 v[36:39], v126 offset:8400
	ds_read_b128 v[40:43], v126 offset:32400
	ds_read_b128 v[44:47], v127 offset:8400
	s_waitcnt lgkmcnt(2)
	v_pk_add_f32 v[32:33], v[32:33], v[36:37]
	v_pk_add_f32 v[34:35], v[34:35], v[38:39]
	s_waitcnt lgkmcnt(1)
	v_pk_add_f32 v[32:33], v[32:33], v[40:41]
	v_pk_add_f32 v[34:35], v[34:35], v[42:43]
	s_waitcnt lgkmcnt(0)
	v_pk_add_f32 v[32:33], v[32:33], v[44:45]
	v_pk_add_f32 v[34:35], v[34:35], v[46:47]
	s_nop 0
	v_cvt_pk_f16_f32 v48, v32, v33
	v_cvt_pk_f16_f32 v49, v34, v35
	global_store_dwordx2 v[116:117], v[48:49], off offset:600
	s_endpgm
.Latt3_fin_hh:
	v_add_u32_e32 v1, 0xfffffd80, v0
	s_movk_i32 s5, 0x4b
	v_cmp_gt_u32_e32 vcc, s5, v1
	s_and_saveexec_b64 s[6:7], vcc
	s_cbranch_execz .Latt3_end
	s_movk_i32 s5, 0xe10
	v_add_u32_e32 v127, 0x112c0, v126
	v_mad_u64_u32 v[110:111], s[8:9], v70, s5, v[100:101]
	v_add_u32_e32 v1, 1, v70
	v_mad_u64_u32 v[112:113], s[8:9], v1, s5, v[100:101]
	v_add_u32_e32 v1, 2, v70
	v_mad_u64_u32 v[114:115], s[8:9], v1, s5, v[100:101]
	v_add_u32_e32 v1, 3, v70
	v_mad_u64_u32 v[116:117], s[8:9], v1, s5, v[100:101]
	ds_read_b128 v[36:39], v126
	ds_read_b128 v[40:43], v126 offset:24000
	ds_read_b128 v[44:47], v127
	s_waitcnt lgkmcnt(2)
	v_pk_add_f32 v[4:5], v[4:5], v[36:37]
	v_pk_add_f32 v[6:7], v[6:7], v[38:39]
	s_waitcnt lgkmcnt(1)
	v_pk_add_f32 v[4:5], v[4:5], v[40:41]
	v_pk_add_f32 v[6:7], v[6:7], v[42:43]
	s_waitcnt lgkmcnt(0)
	v_pk_add_f32 v[4:5], v[4:5], v[44:45]
	v_pk_add_f32 v[6:7], v[6:7], v[46:47]
	s_nop 0
	v_cvt_pk_f16_f32 v48, v4, v5
	v_cvt_pk_f16_f32 v49, v6, v7
	global_store_dwordx2 v[110:111], v[48:49], off
	ds_read_b128 v[36:39], v126 offset:1200
	ds_read_b128 v[40:43], v126 offset:25200
	ds_read_b128 v[44:47], v127 offset:1200
	s_waitcnt lgkmcnt(2)
	v_pk_add_f32 v[8:9], v[8:9], v[36:37]
	v_pk_add_f32 v[10:11], v[10:11], v[38:39]
	s_waitcnt lgkmcnt(1)
	v_pk_add_f32 v[8:9], v[8:9], v[40:41]
	v_pk_add_f32 v[10:11], v[10:11], v[42:43]
	s_waitcnt lgkmcnt(0)
	v_pk_add_f32 v[8:9], v[8:9], v[44:45]
	v_pk_add_f32 v[10:11], v[10:11], v[46:47]
	s_nop 0
	v_cvt_pk_f16_f32 v48, v8, v9
	v_cvt_pk_f16_f32 v49, v10, v11
	global_store_dwordx2 v[112:113], v[48:49], off
	ds_read_b128 v[36:39], v126 offset:2400
	ds_read_b128 v[40:43], v126 offset:26400
	ds_read_b128 v[44:47], v127 offset:2400
	s_waitcnt lgkmcnt(2)
	v_pk_add_f32 v[12:13], v[12:13], v[36:37]
	v_pk_add_f32 v[14:15], v[14:15], v[38:39]
	s_waitcnt lgkmcnt(1)
	v_pk_add_f32 v[12:13], v[12:13], v[40:41]
	v_pk_add_f32 v[14:15], v[14:15], v[42:43]
	s_waitcnt lgkmcnt(0)
	v_pk_add_f32 v[12:13], v[12:13], v[44:45]
	v_pk_add_f32 v[14:15], v[14:15], v[46:47]
	s_nop 0
	v_cvt_pk_f16_f32 v48, v12, v13
	v_cvt_pk_f16_f32 v49, v14, v15
	global_store_dwordx2 v[114:115], v[48:49], off
	ds_read_b128 v[36:39], v126 offset:3600
	ds_read_b128 v[40:43], v126 offset:27600
	ds_read_b128 v[44:47], v127 offset:3600
	s_waitcnt lgkmcnt(2)
	v_pk_add_f32 v[16:17], v[16:17], v[36:37]
	v_pk_add_f32 v[18:19], v[18:19], v[38:39]
	s_waitcnt lgkmcnt(1)
	v_pk_add_f32 v[16:17], v[16:17], v[40:41]
	v_pk_add_f32 v[18:19], v[18:19], v[42:43]
	s_waitcnt lgkmcnt(0)
	v_pk_add_f32 v[16:17], v[16:17], v[44:45]
	v_pk_add_f32 v[18:19], v[18:19], v[46:47]
	s_nop 0
	v_cvt_pk_f16_f32 v48, v16, v17
	v_cvt_pk_f16_f32 v49, v18, v19
	global_store_dwordx2 v[116:117], v[48:49], off

.Latt3_pass:
	v_add_u32_e32 v1, 0xfffffe80, v0
	s_movk_i32 s0, 0x4b
	v_cmp_gt_u32_e32 vcc, s0, v1
	s_and_saveexec_b64 s[0:1], vcc
	s_cbranch_execz .LBB2_39
	v_mov_b32_e32 v1, 0xfffffa00
	v_lshl_add_u32 v8, v0, 2, v1
	v_lshlrev_b32_e32 v14, 2, v8
	ds_read_b128 v[0:3], v14 offset:59392
	ds_read_b128 v[4:7], v14 offset:60608
	v_mov_b32_e32 v9, 0
	s_movk_i32 s2, 0xe10
	v_lshl_add_u64 v[8:9], v[8:9], 1, s[12:13]
	s_waitcnt lgkmcnt(1)
	v_cvt_f16_f32_e32 v0, v0
	v_cvt_f16_f32_e32 v3, v3
	s_waitcnt lgkmcnt(0)
	v_cvt_f16_f32_e32 v4, v4
	v_cvt_f16_f32_e32 v7, v7
	v_cvt_pk_f16_f32 v1, v1, v2
	v_pack_b32_f16 v0, v0, v1
	v_alignbit_b32 v1, v3, v1, 16
	v_mad_u64_u32 v[2:3], s[0:1], v70, s2, v[8:9]
	global_store_dwordx2 v[2:3], v[0:1], off
	v_cvt_pk_f16_f32 v0, v5, v6
	v_pack_b32_f16 v10, v4, v0
	v_alignbit_b32 v11, v7, v0, 16
	ds_read_b128 v[0:3], v14 offset:61824
	v_add_u32_e32 v4, 1, v70
	v_mad_u64_u32 v[12:13], s[0:1], v4, s2, v[8:9]
	ds_read_b128 v[4:7], v14 offset:63040
	s_waitcnt lgkmcnt(1)
	v_cvt_f16_f32_e32 v0, v0
	v_cvt_f16_f32_e32 v3, v3
	v_cvt_pk_f16_f32 v1, v1, v2
	v_add_u32_e32 v2, 2, v70
	s_waitcnt lgkmcnt(0)
	v_cvt_f16_f32_e32 v4, v4
	v_cvt_f16_f32_e32 v7, v7
	v_pack_b32_f16 v0, v0, v1
	v_alignbit_b32 v1, v3, v1, 16
	v_mad_u64_u32 v[2:3], s[0:1], v2, s2, v[8:9]
	global_store_dwordx2 v[2:3], v[0:1], off
	v_cvt_pk_f16_f32 v1, v5, v6
	v_add_u32_e32 v2, 3, v70
	v_pack_b32_f16 v0, v4, v1
	v_alignbit_b32 v1, v7, v1, 16
	v_mad_u64_u32 v[2:3], s[0:1], v2, s2, v[8:9]
	global_store_dwordx2 v[12:13], v[10:11], off
	global_store_dwordx2 v[2:3], v[0:1], off

	.amdhsa_kernel _Z13attend_kernelPKfS0_S0_S0_S0_S0_S0_S0_S0_S0_PDF16_
		.amdhsa_group_segment_fixed_size 94336
		.amdhsa_private_segment_fixed_size 0
		.amdhsa_kernarg_size 88
		.amdhsa_user_sgpr_count 2
		.amdhsa_user_sgpr_dispatch_ptr 0
		.amdhsa_user_sgpr_queue_ptr 0
		.amdhsa_user_sgpr_kernarg_segment_ptr 1
		.amdhsa_user_sgpr_dispatch_id 0
		.amdhsa_user_sgpr_kernarg_preload_length 0
		.amdhsa_user_sgpr_kernarg_preload_offset 0
		.amdhsa_user_sgpr_private_segment_size 0
		.amdhsa_uses_dynamic_stack 0
		.amdhsa_enable_private_segment 0
		.amdhsa_system_sgpr_workgroup_id_x 1
		.amdhsa_system_sgpr_workgroup_id_y 0
		.amdhsa_system_sgpr_workgroup_id_z 0
		.amdhsa_system_sgpr_workgroup_info 0
		.amdhsa_system_vgpr_workitem_id 0
		.amdhsa_next_free_vgpr 128
		.amdhsa_next_free_sgpr 34
		.amdhsa_accum_offset 128
		.amdhsa_reserve_vcc 1
		.amdhsa_float_round_mode_32 0
		.amdhsa_float_round_mode_16_64 0
		.amdhsa_float_denorm_mode_32 3
		.amdhsa_float_denorm_mode_16_64 3
		.amdhsa_dx10_clamp 1
		.amdhsa_ieee_mode 1
		.amdhsa_fp16_overflow 0
		.amdhsa_tg_split 0
		.amdhsa_exception_fp_ieee_invalid_op 0
		.amdhsa_exception_fp_denorm_src 0
		.amdhsa_exception_fp_ieee_div_zero 0
		.amdhsa_exception_fp_ieee_overflow 0
		.amdhsa_exception_fp_ieee_underflow 0
		.amdhsa_exception_fp_ieee_inexact 0
		.amdhsa_exception_int_div_zero 0
	.end_amdhsa_kernel

amdhsa.kernels:
  - .agpr_count:     16
    .args:
      - .actual_access:  read_only
        .address_space:  global
        .offset:         0
        .size:           8
        .value_kind:     global_buffer
      - .actual_access:  read_only
        .address_space:  global
        .offset:         8
        .size:           8
        .value_kind:     global_buffer
      - .actual_access:  read_only
        .address_space:  global
        .offset:         16
        .size:           8
        .value_kind:     global_buffer
      - .actual_access:  read_only
        .address_space:  global
        .offset:         24
        .size:           8
        .value_kind:     global_buffer
      - .actual_access:  write_only
        .address_space:  global
        .offset:         32
        .size:           8
        .value_kind:     global_buffer
      - .offset:         40
        .size:           4
        .value_kind:     by_value
      - .offset:         44
        .size:           4
        .value_kind:     by_value
      - .offset:         48
        .size:           4
        .value_kind:     by_value
      - .offset:         52
        .size:           4
        .value_kind:     by_value
      - .offset:         56
        .size:           4
        .value_kind:     by_value
      - .offset:         60
        .size:           4
        .value_kind:     by_value
      - .offset:         64
        .size:           4
        .value_kind:     by_value
    .group_segment_fixed_size: 43008
    .kernarg_segment_align: 8
    .kernarg_segment_size: 68
    .language:       OpenCL C
    .language_version:
      - 2
      - 0
    .max_flat_workgroup_size: 256
    .name:           _Z15gemm_f16_kernelPKDF16_S0_PKfS2_Pfiiiiiii
    .private_segment_fixed_size: 0
    .sgpr_count:     33
    .sgpr_spill_count: 0
    .symbol:         _Z15gemm_f16_kernelPKDF16_S0_PKfS2_Pfiiiiiii.kd
    .uniform_work_group_size: 1
    .uses_dynamic_stack: false
    .vgpr_count:     152
    .vgpr_spill_count: 0
    .wavefront_size: 64
  - .agpr_count:     0
    .args:
      - .actual_access:  read_only
        .address_space:  global
        .offset:         0
        .size:           8
        .value_kind:     global_buffer
      - .actual_access:  read_only
        .address_space:  global
        .offset:         8
        .size:           8
        .value_kind:     global_buffer
      - .actual_access:  read_only
        .address_space:  global
        .offset:         16
        .size:           8
        .value_kind:     global_buffer
      - .actual_access:  read_only
        .address_space:  global
        .offset:         24
        .size:           8
        .value_kind:     global_buffer
      - .actual_access:  read_only
        .address_space:  global
        .offset:         32
        .size:           8
        .value_kind:     global_buffer
      - .actual_access:  read_only
        .address_space:  global
        .offset:         40
        .size:           8
        .value_kind:     global_buffer
      - .actual_access:  write_only
        .address_space:  global
        .offset:         48
        .size:           8
        .value_kind:     global_buffer
      - .actual_access:  read_only
        .address_space:  global
        .offset:         56
        .size:           8
        .value_kind:     global_buffer
    .group_segment_fixed_size: 121472
    .kernarg_segment_align: 8
    .kernarg_segment_size: 64
    .language:       OpenCL C
    .language_version:
      - 2
      - 0
    .max_flat_workgroup_size: 512
    .name:           _Z15score_ds_kernelPKfS0_S0_S0_S0_S0_PfPKDF16_
    .private_segment_fixed_size: 0
    .sgpr_count:     32
    .sgpr_spill_count: 0
    .symbol:         _Z15score_ds_kernelPKfS0_S0_S0_S0_S0_PfPKDF16_.kd
    .uniform_work_group_size: 1
    .uses_dynamic_stack: false
    .vgpr_count:     254
    .vgpr_spill_count: 0
    .wavefront_size: 64
  - .agpr_count:     0
    .args:
      - .actual_access:  read_only
        .address_space:  global
        .offset:         0
        .size:           8
        .value_kind:     global_buffer
      - .actual_access:  read_only
        .address_space:  global
        .offset:         8
        .size:           8
        .value_kind:     global_buffer
      - .actual_access:  read_only
        .address_space:  global
        .offset:         16
        .size:           8
        .value_kind:     global_buffer
      - .actual_access:  read_only
        .address_space:  global
        .offset:         24
        .size:           8
        .value_kind:     global_buffer
      - .actual_access:  read_only
        .address_space:  global
        .offset:         32
        .size:           8
        .value_kind:     global_buffer
      - .actual_access:  read_only
        .address_space:  global
        .offset:         40
        .size:           8
        .value_kind:     global_buffer
      - .actual_access:  read_only
        .address_space:  global
        .offset:         48
        .size:           8
        .value_kind:     global_buffer
      - .actual_access:  read_only
        .address_space:  global
        .offset:         56
        .size:           8
        .value_kind:     global_buffer
      - .actual_access:  read_only
        .address_space:  global
        .offset:         64
        .size:           8
        .value_kind:     global_buffer
      - .actual_access:  read_only
        .address_space:  global
        .offset:         72
        .size:           8
        .value_kind:     global_buffer
      - .actual_access:  write_only
        .address_space:  global
        .offset:         80
        .size:           8
        .value_kind:     global_buffer
    .group_segment_fixed_size: 94336
    .kernarg_segment_align: 8
    .kernarg_segment_size: 88
    .language:       OpenCL C
    .language_version:
      - 2
      - 0
    .max_flat_workgroup_size: 1024
    .name:           _Z13attend_kernelPKfS0_S0_S0_S0_S0_S0_S0_S0_S0_PDF16_
    .private_segment_fixed_size: 0
    .sgpr_count:     40
    .sgpr_spill_count: 0
    .symbol:         _Z13attend_kernelPKfS0_S0_S0_S0_S0_S0_S0_S0_S0_PDF16_.kd
    .uniform_work_group_size: 1
    .uses_dynamic_stack: false
    .vgpr_count:     128
    .vgpr_spill_count: 0
    .wavefront_size: 64
  - .agpr_count:     0
    .args:
      - .actual_access:  read_only
        .address_space:  global
        .offset:         0
        .size:           8
        .value_kind:     global_buffer
      - .actual_access:  read_only
        .address_space:  global
        .offset:         8
        .size:           8
        .value_kind:     global_buffer
      - .actual_access:  read_only
        .address_space:  global
        .offset:         16
        .size:           8
        .value_kind:     global_buffer
      - .actual_access:  read_only
        .address_space:  global
        .offset:         24
        .size:           8
        .value_kind:     global_buffer
      - .actual_access:  write_only
        .address_space:  global
        .offset:         32
        .size:           8
        .value_kind:     global_buffer
    .group_segment_fixed_size: 9088
    .kernarg_segment_align: 8
    .kernarg_segment_size: 40
    .language:       OpenCL C
    .language_version:
      - 2
      - 0
    .max_flat_workgroup_size: 512
    .name:           _Z16postfinal_kernelPKfS0_S0_S0_Pf
    .private_segment_fixed_size: 0
    .sgpr_count:     30
    .sgpr_spill_count: 0
    .symbol:         _Z16postfinal_kernelPKfS0_S0_S0_Pf.kd
    .uniform_work_group_size: 1
    .uses_dynamic_stack: false
    .vgpr_count:     124
    .vgpr_spill_count: 0
    .wavefront_size: 64
  - .agpr_count:     16
    .args:
      - .offset:         0
        .size:           1136
        .value_kind:     by_value
    .group_segment_fixed_size: 34816
    .kernarg_segment_align: 8
    .kernarg_segment_size: 1136
    .language:       OpenCL C
    .language_version:
      - 2
      - 0
    .max_flat_workgroup_size: 256
    .name:           _Z14gemm_nt_kernelILi2EEv8GemmArgs
    .private_segment_fixed_size: 0
    .sgpr_count:     68
    .sgpr_spill_count: 0
    .symbol:         _Z14gemm_nt_kernelILi2EEv8GemmArgs.kd
    .uniform_work_group_size: 1
    .uses_dynamic_stack: false
    .vgpr_count:     140
    .vgpr_spill_count: 0
    .wavefront_size: 64
  - .agpr_count:     0
    .args:
      - .actual_access:  read_only
        .address_space:  global
        .offset:         0
        .size:           8
        .value_kind:     global_buffer
      - .offset:         8
        .size:           8
        .value_kind:     by_value
      - .actual_access:  read_only
        .address_space:  global
        .offset:         16
        .size:           8
        .value_kind:     global_buffer
      - .actual_access:  read_only
        .address_space:  global
        .offset:         24
        .size:           8
        .value_kind:     global_buffer
      - .actual_access:  read_only
        .address_space:  global
        .offset:         32
        .size:           8
        .value_kind:     global_buffer
      - .actual_access:  read_only
        .address_space:  global
        .offset:         40
        .size:           8
        .value_kind:     global_buffer
      - .actual_access:  write_only
        .address_space:  global
        .offset:         48
        .size:           8
        .value_kind:     global_buffer
      - .actual_access:  write_only
        .address_space:  global
        .offset:         56
        .size:           8
        .value_kind:     global_buffer
      - .offset:         64
        .size:           4
        .value_kind:     by_value
      - .offset:         72
        .size:           376
        .value_kind:     by_value
    .group_segment_fixed_size: 63488
    .kernarg_segment_align: 8
    .kernarg_segment_size: 448
    .language:       OpenCL C
    .language_version:
      - 2
      - 0
    .max_flat_workgroup_size: 512
    .name:           _Z15gru_mfma_kernelILi1EEvPKfmS1_S1_S1_S1_PfS2_i7PreArgs
    .private_segment_fixed_size: 0
    .sgpr_count:     36
    .sgpr_spill_count: 0
    .symbol:         _Z15gru_mfma_kernelILi1EEvPKfmS1_S1_S1_S1_PfS2_i7PreArgs.kd
    .uniform_work_group_size: 1
    .uses_dynamic_stack: false
    .vgpr_count:     232
    .vgpr_spill_count: 0
    .wavefront_size: 64
  - .agpr_count:     0
    .args:
      - .actual_access:  read_only
        .address_space:  global
        .offset:         0
        .size:           8
        .value_kind:     global_buffer
      - .offset:         8
        .size:           8
        .value_kind:     by_value
      - .actual_access:  read_only
        .address_space:  global
        .offset:         16
        .size:           8
        .value_kind:     global_buffer
      - .actual_access:  read_only
        .address_space:  global
        .offset:         24
        .size:           8
        .value_kind:     global_buffer
      - .actual_access:  read_only
        .address_space:  global
        .offset:         32
        .size:           8
        .value_kind:     global_buffer
      - .actual_access:  read_only
        .address_space:  global
        .offset:         40
        .size:           8
        .value_kind:     global_buffer
      - .actual_access:  write_only
        .address_space:  global
        .offset:         48
        .size:           8
        .value_kind:     global_buffer
      - .actual_access:  write_only
        .address_space:  global
        .offset:         56
        .size:           8
        .value_kind:     global_buffer
      - .offset:         64
        .size:           4
        .value_kind:     by_value
      - .offset:         72
        .size:           376
        .value_kind:     by_value
    .group_segment_fixed_size: 64480
    .kernarg_segment_align: 8
    .kernarg_segment_size: 448
    .language:       OpenCL C
    .language_version:
      - 2
      - 0
    .max_flat_workgroup_size: 512
    .name:           _Z15gru_mfma_kernelILi2EEvPKfmS1_S1_S1_S1_PfS2_i7PreArgs
    .private_segment_fixed_size: 0
    .sgpr_count:     50
    .sgpr_spill_count: 0
    .symbol:         _Z15gru_mfma_kernelILi2EEvPKfmS1_S1_S1_S1_PfS2_i7PreArgs.kd
    .uniform_work_group_size: 1
    .uses_dynamic_stack: false
    .vgpr_count:     232
    .vgpr_spill_count: 0
    .wavefront_size: 64
